# gemm: separate loop copies for waves 0-3 / 4-7 with LDS-DMA issue slots offset by 3 MFMAs (partner-wave DMA de-phasing)
# baseline (speedup 1.0000x reference)
_Z8gemm_qkvPKDF16_S0_PKfPDF16_S3_S3_Pj:
	v_readfirstlane_b32 s13, v0
	s_lshr_b32 s8, s13, 6
	v_bfe_u32 v2, v0, 3, 3
	s_load_dwordx4 s[4:7], s[0:1], 0x0
	v_lshl_or_b32 v6, s8, 3, v2
	v_lshrrev_b32_e32 v2, 1, v6
	s_mul_i32 s16, s3, 0xc0
	v_xor_b32_e32 v4, v2, v0
	v_add_u32_e32 v2, s16, v6
	v_ashrrev_i32_e32 v3, 31, v2
	s_bfe_u32 s15, s13, 0x20006
	v_lshlrev_b64 v[2:3], 11, v[2:3]
	v_lshlrev_b32_e32 v4, 4, v4
	s_mul_i32 s10, s2, 0xc0
	s_mul_i32 s2, s15, 48
	s_waitcnt lgkmcnt(0)
	v_lshl_add_u64 v[2:3], s[4:5], 0, v[2:3]
	v_and_b32_e32 v4, 0x70, v4
	v_mov_b32_e32 v5, 0
	s_add_i32 s17, s2, s10
	v_lshl_add_u64 v[218:219], v[2:3], 0, v[4:5]
	v_add_u32_e32 v2, s10, v6
	s_lshl_b32 s8, s8, 10
	v_ashrrev_i32_e32 v3, 31, v2
	s_cmp_lg_u32 0x400, -1
	v_lshlrev_b64 v[2:3], 11, v[2:3]
	s_cselect_b32 s4, 0x400, 0
	v_lshl_add_u64 v[2:3], s[6:7], 0, v[2:3]
	s_add_i32 s11, s8, s4
	s_mov_b32 s4, m0
	s_mov_b32 m0, s11
	s_nop 0
	global_load_lds_dwordx4 v[218:219], off
	s_mov_b32 m0, s4
	v_lshl_add_u64 v[220:221], v[2:3], 0, v[4:5]
	s_add_i32 s4, s11, 0x6000
	s_mov_b32 s5, m0
	s_mov_b32 m0, s4
	s_nop 0
	global_load_lds_dwordx4 v[220:221], off
	s_mov_b32 m0, s5
	s_mov_b64 s[4:5], 0x20000
	v_lshl_add_u64 v[222:223], v[218:219], 0, s[4:5]
	s_add_i32 s9, s11, 0x2000
	s_mov_b32 s6, m0
	s_mov_b32 m0, s9
	s_nop 0
	global_load_lds_dwordx4 v[222:223], off
	s_mov_b32 m0, s6
	v_lshl_add_u64 v[224:225], v[220:221], 0, s[4:5]
	s_add_i32 s4, s11, 0x8000
	s_mov_b32 s5, m0
	s_mov_b32 m0, s4
	s_nop 0
	global_load_lds_dwordx4 v[224:225], off
	s_mov_b32 m0, s5
	s_mov_b64 s[4:5], 0x40000
	v_lshl_add_u64 v[226:227], v[218:219], 0, s[4:5]
	s_add_i32 s12, s11, 0x4000
	s_mov_b32 s6, m0
	s_mov_b32 m0, s12
	s_nop 0
	global_load_lds_dwordx4 v[226:227], off
	s_mov_b32 m0, s6
	v_lshl_add_u64 v[228:229], v[220:221], 0, s[4:5]
	s_add_i32 s4, s11, 0xa000
	s_mov_b32 s5, m0
	s_mov_b32 m0, s4
	s_nop 0
	global_load_lds_dwordx4 v[228:229], off
	s_mov_b32 m0, s5
	s_cmpk_gt_i32 s17, 0x7d0
	s_cselect_b64 s[4:5], -1, 0
	s_lshr_b32 s14, s13, 8
	s_mul_i32 s6, s14, 0x3000
	s_add_i32 s13, s6, 0x400
	s_mov_b64 s[6:7], 0x80
	s_add_i32 s18, s11, 0xc000
	v_lshl_add_u64 v[2:3], v[218:219], 0, s[6:7]
	s_mov_b32 s30, m0
	s_mov_b32 m0, s18
	s_nop 0
	global_load_lds_dwordx4 v[2:3], off
	s_mov_b32 m0, s30
	s_add_i32 s19, s11, 0x12000
	v_lshl_add_u64 v[2:3], v[220:221], 0, s[6:7]
	s_mov_b32 s6, m0
	s_mov_b32 m0, s19
	s_nop 0
	global_load_lds_dwordx4 v[2:3], off
	s_mov_b32 m0, s6
	s_mov_b64 s[6:7], 0x20080
	s_add_i32 s20, s11, 0xe000
	v_lshl_add_u64 v[2:3], v[218:219], 0, s[6:7]
	s_mov_b32 s18, m0
	s_mov_b32 m0, s20
	s_nop 0
	global_load_lds_dwordx4 v[2:3], off
	s_mov_b32 m0, s18
	s_add_i32 s21, s11, 0x14000
	v_lshl_add_u64 v[2:3], v[220:221], 0, s[6:7]
	s_mov_b32 s6, m0
	s_mov_b32 m0, s21
	s_nop 0
	global_load_lds_dwordx4 v[2:3], off
	s_mov_b32 m0, s6
	s_mov_b64 s[6:7], 0x40080
	v_lshl_add_u64 v[2:3], v[218:219], 0, s[6:7]
	s_add_i32 s22, s11, 0x10000
	s_mov_b32 s18, m0
	s_mov_b32 m0, s22
	s_nop 0
	global_load_lds_dwordx4 v[2:3], off
	s_mov_b32 m0, s18
	v_lshl_add_u64 v[2:3], v[220:221], 0, s[6:7]
	v_and_b32_e32 v1, 15, v0
	v_bfe_u32 v231, v0, 4, 2
	s_add_i32 s23, s11, 0x16000
	s_mov_b32 s6, m0
	s_mov_b32 m0, s23
	s_nop 0
	global_load_lds_dwordx4 v[2:3], off
	s_mov_b32 m0, s6
	v_lshrrev_b32_e32 v3, 1, v0
	v_lshlrev_b32_e32 v2, 7, v1
	v_bfe_u32 v4, v0, 1, 3
	v_bitop3_b32 v3, v231, v3, 7 bitop3:0x78
	v_lshl_or_b32 v238, v3, 4, v2
	v_bitop3_b32 v3, v231, v4, 4 bitop3:0x36
	v_lshl_or_b32 v240, v3, 4, v2
	s_mulk_i32 s15, 0x1800
	s_addk_i32 s15, 0x6400
	v_add_u32_e32 v158, s13, v238
	v_add_u32_e32 v160, s13, v240
	v_add_u32_e32 v162, s15, v238
	v_add_u32_e32 v164, s15, v240
	s_add_u32 m0, s11, 0x17f00
	s_nop 0
	global_load_lds_dwordx4 v[218:219], off offset:256
	s_add_u32 m0, s11, 0x19f00
	s_nop 0
	global_load_lds_dwordx4 v[222:223], off offset:256
	s_add_u32 m0, s11, 0x1bf00
	s_nop 0
	global_load_lds_dwordx4 v[226:227], off offset:256
	s_load_dwordx2 s[24:25], s[0:1], 0x10
	s_mov_b32 s20, 0x180
	s_mov_b32 s21, 0
	v_lshl_add_u64 v[218:219], v[218:219], 0, s[20:21]
	v_lshl_add_u64 v[222:223], v[222:223], 0, s[20:21]
	v_lshl_add_u64 v[226:227], v[226:227], 0, s[20:21]
	v_lshl_add_u64 v[220:221], v[220:221], 0, s[20:21]
	v_lshl_add_u64 v[224:225], v[224:225], 0, s[20:21]
	v_lshl_add_u64 v[228:229], v[228:229], 0, s[20:21]
	v_add_u32_e32 v159, 0x18000, v158
	v_add_u32_e32 v161, 0x18000, v160
	v_add_u32_e32 v163, 0x18000, v162
	v_add_u32_e32 v165, 0x18000, v164
	v_mov_b32_e32 v82, 0
	v_mov_b32_e32 v83, 0
	v_mov_b32_e32 v84, 0
	v_mov_b32_e32 v85, 0
	v_mov_b32_e32 v58, 0
	v_mov_b32_e32 v59, 0
	v_mov_b32_e32 v60, 0
	v_mov_b32_e32 v61, 0
	v_mov_b32_e32 v14, 0
	v_mov_b32_e32 v15, 0
	v_mov_b32_e32 v16, 0
	v_mov_b32_e32 v17, 0
	v_mov_b32_e32 v78, 0
	v_mov_b32_e32 v79, 0
	v_mov_b32_e32 v80, 0
	v_mov_b32_e32 v81, 0
	v_mov_b32_e32 v22, 0
	v_mov_b32_e32 v23, 0
	v_mov_b32_e32 v24, 0
	v_mov_b32_e32 v25, 0
	v_mov_b32_e32 v30, 0
	v_mov_b32_e32 v31, 0
	v_mov_b32_e32 v32, 0
	v_mov_b32_e32 v33, 0
	v_mov_b32_e32 v74, 0
	v_mov_b32_e32 v75, 0
	v_mov_b32_e32 v76, 0
	v_mov_b32_e32 v77, 0
	v_mov_b32_e32 v18, 0
	v_mov_b32_e32 v19, 0
	v_mov_b32_e32 v20, 0
	v_mov_b32_e32 v21, 0
	v_mov_b32_e32 v26, 0
	v_mov_b32_e32 v27, 0
	v_mov_b32_e32 v28, 0
	v_mov_b32_e32 v29, 0
	v_mov_b32_e32 v70, 0
	v_mov_b32_e32 v71, 0
	v_mov_b32_e32 v72, 0
	v_mov_b32_e32 v73, 0
	v_mov_b32_e32 v46, 0
	v_mov_b32_e32 v47, 0
	v_mov_b32_e32 v48, 0
	v_mov_b32_e32 v49, 0
	v_mov_b32_e32 v240, 0
	v_mov_b32_e32 v241, 0
	v_mov_b32_e32 v242, 0
	v_mov_b32_e32 v243, 0
	v_mov_b32_e32 v66, 0
	v_mov_b32_e32 v67, 0
	v_mov_b32_e32 v68, 0
	v_mov_b32_e32 v69, 0
	v_mov_b32_e32 v42, 0
	v_mov_b32_e32 v43, 0
	v_mov_b32_e32 v44, 0
	v_mov_b32_e32 v45, 0
	v_mov_b32_e32 v236, 0
	v_mov_b32_e32 v237, 0
	v_mov_b32_e32 v238, 0
	v_mov_b32_e32 v239, 0
	v_mov_b32_e32 v62, 0
	v_mov_b32_e32 v63, 0
	v_mov_b32_e32 v64, 0
	v_mov_b32_e32 v65, 0
	v_mov_b32_e32 v38, 0
	v_mov_b32_e32 v39, 0
	v_mov_b32_e32 v40, 0
	v_mov_b32_e32 v41, 0
	v_mov_b32_e32 v34, 0
	v_mov_b32_e32 v35, 0
	v_mov_b32_e32 v36, 0
	v_mov_b32_e32 v37, 0
	s_not_b64 s[6:7], s[4:5]
	s_mov_b32 s22, 4
	s_waitcnt vmcnt(9) lgkmcnt(0)
	s_barrier
	ds_read_b128 v[134:137], v162
	ds_read_b128 v[138:141], v162 offset:2048
	ds_read_b128 v[142:145], v162 offset:4096
	ds_read_b128 v[86:89], v158
	ds_read_b128 v[90:93], v158 offset:2048
	ds_read_b128 v[94:97], v158 offset:4096
	ds_read_b128 v[98:101], v158 offset:6144
	ds_read_b128 v[102:105], v158 offset:8192
	ds_read_b128 v[106:109], v158 offset:10240
	ds_read_b128 v[110:113], v160
	ds_read_b128 v[114:117], v160 offset:2048
	ds_read_b128 v[118:121], v160 offset:4096
	ds_read_b128 v[122:125], v160 offset:6144
	ds_read_b128 v[126:129], v160 offset:8192
	ds_read_b128 v[130:133], v160 offset:10240
	ds_read_b128 v[146:149], v164
	ds_read_b128 v[150:153], v164 offset:2048
	ds_read_b128 v[154:157], v164 offset:4096
	s_and_b64 vcc, exec, s[4:5]
	s_cbranch_vccnz .Lgemm_N_entry
	s_cmp_lg_u32 s14, 0
	s_cbranch_scc1 .Lgemm_Th_loop

.Lgemm_Th_loop:
	s_waitcnt lgkmcnt(9)
	v_mfma_f32_16x16x32_f16 v[82:85], v[134:137], v[86:89], v[82:85]
	v_mfma_f32_16x16x32_f16 v[58:61], v[138:141], v[86:89], v[58:61]
	v_mfma_f32_16x16x32_f16 v[14:17], v[142:145], v[86:89], v[14:17]
	s_add_u32 m0, s11, 0x1e080
	v_mfma_f32_16x16x32_f16 v[78:81], v[134:137], v[90:93], v[78:81]
	global_load_lds_dwordx4 v[220:221], off offset:-128
	v_mfma_f32_16x16x32_f16 v[22:25], v[138:141], v[90:93], v[22:25]
	v_mfma_f32_16x16x32_f16 v[30:33], v[142:145], v[90:93], v[30:33]
	v_mfma_f32_16x16x32_f16 v[74:77], v[134:137], v[94:97], v[74:77]
	v_mfma_f32_16x16x32_f16 v[18:21], v[138:141], v[94:97], v[18:21]
	v_mfma_f32_16x16x32_f16 v[26:29], v[142:145], v[94:97], v[26:29]
	s_add_u32 m0, s11, 0x20080
	v_mfma_f32_16x16x32_f16 v[70:73], v[134:137], v[98:101], v[70:73]
	global_load_lds_dwordx4 v[224:225], off offset:-128
	v_mfma_f32_16x16x32_f16 v[46:49], v[138:141], v[98:101], v[46:49]
	v_mfma_f32_16x16x32_f16 v[240:243], v[142:145], v[98:101], v[240:243]
	v_mfma_f32_16x16x32_f16 v[66:69], v[134:137], v[102:105], v[66:69]
	v_mfma_f32_16x16x32_f16 v[42:45], v[138:141], v[102:105], v[42:45]
	v_mfma_f32_16x16x32_f16 v[236:239], v[142:145], v[102:105], v[236:239]
	s_add_u32 m0, s11, 0x22080
	v_mfma_f32_16x16x32_f16 v[62:65], v[134:137], v[106:109], v[62:65]
	global_load_lds_dwordx4 v[228:229], off offset:-128
	v_mfma_f32_16x16x32_f16 v[38:41], v[138:141], v[106:109], v[38:41]
	v_mfma_f32_16x16x32_f16 v[34:37], v[142:145], v[106:109], v[34:37]
	s_waitcnt vmcnt(6) lgkmcnt(0)
	s_barrier
	ds_read_b128 v[134:137], v162 offset:49152
	v_mfma_f32_16x16x32_f16 v[82:85], v[146:149], v[110:113], v[82:85]
	ds_read_b128 v[138:141], v162 offset:51200
	v_mfma_f32_16x16x32_f16 v[58:61], v[150:153], v[110:113], v[58:61]
	ds_read_b128 v[142:145], v162 offset:53248
	v_mfma_f32_16x16x32_f16 v[14:17], v[154:157], v[110:113], v[14:17]
	s_add_u32 m0, s11, 0x0
	ds_read_b128 v[86:89], v158 offset:49152
	global_load_lds_dwordx4 v[218:219], off
	v_mfma_f32_16x16x32_f16 v[78:81], v[146:149], v[114:117], v[78:81]
	ds_read_b128 v[90:93], v158 offset:51200
	v_mfma_f32_16x16x32_f16 v[22:25], v[150:153], v[114:117], v[22:25]
	ds_read_b128 v[94:97], v158 offset:53248
	v_mfma_f32_16x16x32_f16 v[30:33], v[154:157], v[114:117], v[30:33]
	ds_read_b128 v[98:101], v158 offset:55296
	v_mfma_f32_16x16x32_f16 v[74:77], v[146:149], v[118:121], v[74:77]
	ds_read_b128 v[102:105], v158 offset:57344
	v_mfma_f32_16x16x32_f16 v[18:21], v[150:153], v[118:121], v[18:21]
	ds_read_b128 v[106:109], v158 offset:59392
	v_mfma_f32_16x16x32_f16 v[26:29], v[154:157], v[118:121], v[26:29]
	s_add_u32 m0, s11, 0x2000
	ds_read_b128 v[110:113], v160 offset:49152
	global_load_lds_dwordx4 v[222:223], off
	v_mfma_f32_16x16x32_f16 v[70:73], v[146:149], v[122:125], v[70:73]
	ds_read_b128 v[114:117], v160 offset:51200
	v_mfma_f32_16x16x32_f16 v[46:49], v[150:153], v[122:125], v[46:49]
	v_mfma_f32_16x16x32_f16 v[240:243], v[154:157], v[122:125], v[240:243]
	ds_read_b128 v[118:121], v160 offset:53248
	v_mfma_f32_16x16x32_f16 v[66:69], v[146:149], v[126:129], v[66:69]
	ds_read_b128 v[122:125], v160 offset:55296
	v_mfma_f32_16x16x32_f16 v[42:45], v[150:153], v[126:129], v[42:45]
	v_mfma_f32_16x16x32_f16 v[236:239], v[154:157], v[126:129], v[236:239]
	s_add_u32 m0, s11, 0x4000
	ds_read_b128 v[126:129], v160 offset:57344
	global_load_lds_dwordx4 v[226:227], off
	v_mfma_f32_16x16x32_f16 v[62:65], v[146:149], v[130:133], v[62:65]
	v_mfma_f32_16x16x32_f16 v[38:41], v[150:153], v[130:133], v[38:41]
	v_mfma_f32_16x16x32_f16 v[34:37], v[154:157], v[130:133], v[34:37]
	ds_read_b128 v[130:133], v160 offset:59392
	ds_read_b128 v[146:149], v164 offset:49152
	ds_read_b128 v[150:153], v164 offset:51200
	ds_read_b128 v[154:157], v164 offset:53248
	s_waitcnt lgkmcnt(9)
	v_mfma_f32_16x16x32_f16 v[82:85], v[134:137], v[86:89], v[82:85]
	v_mfma_f32_16x16x32_f16 v[58:61], v[138:141], v[86:89], v[58:61]
	v_mfma_f32_16x16x32_f16 v[14:17], v[142:145], v[86:89], v[14:17]
	s_add_u32 m0, s11, 0x6000
	v_mfma_f32_16x16x32_f16 v[78:81], v[134:137], v[90:93], v[78:81]
	global_load_lds_dwordx4 v[220:221], off
	v_mfma_f32_16x16x32_f16 v[22:25], v[138:141], v[90:93], v[22:25]
	v_mfma_f32_16x16x32_f16 v[30:33], v[142:145], v[90:93], v[30:33]
	v_mfma_f32_16x16x32_f16 v[74:77], v[134:137], v[94:97], v[74:77]
	v_mfma_f32_16x16x32_f16 v[18:21], v[138:141], v[94:97], v[18:21]
	v_mfma_f32_16x16x32_f16 v[26:29], v[142:145], v[94:97], v[26:29]
	s_add_u32 m0, s11, 0x8000
	v_mfma_f32_16x16x32_f16 v[70:73], v[134:137], v[98:101], v[70:73]
	global_load_lds_dwordx4 v[224:225], off
	v_mfma_f32_16x16x32_f16 v[46:49], v[138:141], v[98:101], v[46:49]
	v_mfma_f32_16x16x32_f16 v[240:243], v[142:145], v[98:101], v[240:243]
	v_mfma_f32_16x16x32_f16 v[66:69], v[134:137], v[102:105], v[66:69]
	v_mfma_f32_16x16x32_f16 v[42:45], v[138:141], v[102:105], v[42:45]
	v_mfma_f32_16x16x32_f16 v[236:239], v[142:145], v[102:105], v[236:239]
	s_add_u32 m0, s11, 0xa000
	v_mfma_f32_16x16x32_f16 v[62:65], v[134:137], v[106:109], v[62:65]
	global_load_lds_dwordx4 v[228:229], off
	v_mfma_f32_16x16x32_f16 v[38:41], v[138:141], v[106:109], v[38:41]
	v_mfma_f32_16x16x32_f16 v[34:37], v[142:145], v[106:109], v[34:37]
	s_waitcnt vmcnt(6) lgkmcnt(0)
	s_barrier
	ds_read_b128 v[134:137], v163
	v_mfma_f32_16x16x32_f16 v[82:85], v[146:149], v[110:113], v[82:85]
	ds_read_b128 v[138:141], v163 offset:2048
	v_mfma_f32_16x16x32_f16 v[58:61], v[150:153], v[110:113], v[58:61]
	ds_read_b128 v[142:145], v163 offset:4096
	v_mfma_f32_16x16x32_f16 v[14:17], v[154:157], v[110:113], v[14:17]
	s_add_u32 m0, s11, 0xbf80
	ds_read_b128 v[86:89], v159
	global_load_lds_dwordx4 v[218:219], off offset:128
	v_mfma_f32_16x16x32_f16 v[78:81], v[146:149], v[114:117], v[78:81]
	ds_read_b128 v[90:93], v159 offset:2048
	v_mfma_f32_16x16x32_f16 v[22:25], v[150:153], v[114:117], v[22:25]
	ds_read_b128 v[94:97], v159 offset:4096
	v_mfma_f32_16x16x32_f16 v[30:33], v[154:157], v[114:117], v[30:33]
	ds_read_b128 v[98:101], v159 offset:6144
	v_mfma_f32_16x16x32_f16 v[74:77], v[146:149], v[118:121], v[74:77]
	ds_read_b128 v[102:105], v159 offset:8192
	v_mfma_f32_16x16x32_f16 v[18:21], v[150:153], v[118:121], v[18:21]
	ds_read_b128 v[106:109], v159 offset:10240
	v_mfma_f32_16x16x32_f16 v[26:29], v[154:157], v[118:121], v[26:29]
	s_add_u32 m0, s11, 0xdf80
	ds_read_b128 v[110:113], v161
	global_load_lds_dwordx4 v[222:223], off offset:128
	v_mfma_f32_16x16x32_f16 v[70:73], v[146:149], v[122:125], v[70:73]
	ds_read_b128 v[114:117], v161 offset:2048
	v_mfma_f32_16x16x32_f16 v[46:49], v[150:153], v[122:125], v[46:49]
	v_mfma_f32_16x16x32_f16 v[240:243], v[154:157], v[122:125], v[240:243]
	ds_read_b128 v[118:121], v161 offset:4096
	v_mfma_f32_16x16x32_f16 v[66:69], v[146:149], v[126:129], v[66:69]
	ds_read_b128 v[122:125], v161 offset:6144
	v_mfma_f32_16x16x32_f16 v[42:45], v[150:153], v[126:129], v[42:45]
	v_mfma_f32_16x16x32_f16 v[236:239], v[154:157], v[126:129], v[236:239]
	s_add_u32 m0, s11, 0xff80
	ds_read_b128 v[126:129], v161 offset:8192
	global_load_lds_dwordx4 v[226:227], off offset:128
	v_mfma_f32_16x16x32_f16 v[62:65], v[146:149], v[130:133], v[62:65]
	v_mfma_f32_16x16x32_f16 v[38:41], v[150:153], v[130:133], v[38:41]
	v_mfma_f32_16x16x32_f16 v[34:37], v[154:157], v[130:133], v[34:37]
	ds_read_b128 v[130:133], v161 offset:10240
	ds_read_b128 v[146:149], v165
	ds_read_b128 v[150:153], v165 offset:2048
	ds_read_b128 v[154:157], v165 offset:4096
	s_waitcnt lgkmcnt(9)
	v_mfma_f32_16x16x32_f16 v[82:85], v[134:137], v[86:89], v[82:85]
	v_mfma_f32_16x16x32_f16 v[58:61], v[138:141], v[86:89], v[58:61]
	v_mfma_f32_16x16x32_f16 v[14:17], v[142:145], v[86:89], v[14:17]
	s_add_u32 m0, s11, 0x11f80
	v_mfma_f32_16x16x32_f16 v[78:81], v[134:137], v[90:93], v[78:81]
	global_load_lds_dwordx4 v[220:221], off offset:128
	v_mfma_f32_16x16x32_f16 v[22:25], v[138:141], v[90:93], v[22:25]
	v_mfma_f32_16x16x32_f16 v[30:33], v[142:145], v[90:93], v[30:33]
	v_mfma_f32_16x16x32_f16 v[74:77], v[134:137], v[94:97], v[74:77]
	v_mfma_f32_16x16x32_f16 v[18:21], v[138:141], v[94:97], v[18:21]
	v_mfma_f32_16x16x32_f16 v[26:29], v[142:145], v[94:97], v[26:29]
	s_add_u32 m0, s11, 0x13f80
	v_mfma_f32_16x16x32_f16 v[70:73], v[134:137], v[98:101], v[70:73]
	global_load_lds_dwordx4 v[224:225], off offset:128
	v_mfma_f32_16x16x32_f16 v[46:49], v[138:141], v[98:101], v[46:49]
	v_mfma_f32_16x16x32_f16 v[240:243], v[142:145], v[98:101], v[240:243]
	v_mfma_f32_16x16x32_f16 v[66:69], v[134:137], v[102:105], v[66:69]
	v_mfma_f32_16x16x32_f16 v[42:45], v[138:141], v[102:105], v[42:45]
	v_mfma_f32_16x16x32_f16 v[236:239], v[142:145], v[102:105], v[236:239]
	s_add_u32 m0, s11, 0x15f80
	v_mfma_f32_16x16x32_f16 v[62:65], v[134:137], v[106:109], v[62:65]
	global_load_lds_dwordx4 v[228:229], off offset:128
	v_mfma_f32_16x16x32_f16 v[38:41], v[138:141], v[106:109], v[38:41]
	v_mfma_f32_16x16x32_f16 v[34:37], v[142:145], v[106:109], v[34:37]
	s_waitcnt vmcnt(6) lgkmcnt(0)
	s_barrier
	ds_read_b128 v[134:137], v162
	v_mfma_f32_16x16x32_f16 v[82:85], v[146:149], v[110:113], v[82:85]
	ds_read_b128 v[138:141], v162 offset:2048
	v_mfma_f32_16x16x32_f16 v[58:61], v[150:153], v[110:113], v[58:61]
	ds_read_b128 v[142:145], v162 offset:4096
	v_mfma_f32_16x16x32_f16 v[14:17], v[154:157], v[110:113], v[14:17]
	s_add_u32 m0, s11, 0x17f00
	ds_read_b128 v[86:89], v158
	global_load_lds_dwordx4 v[218:219], off offset:256
	v_mfma_f32_16x16x32_f16 v[78:81], v[146:149], v[114:117], v[78:81]
	ds_read_b128 v[90:93], v158 offset:2048
	v_mfma_f32_16x16x32_f16 v[22:25], v[150:153], v[114:117], v[22:25]
	ds_read_b128 v[94:97], v158 offset:4096
	v_mfma_f32_16x16x32_f16 v[30:33], v[154:157], v[114:117], v[30:33]
	ds_read_b128 v[98:101], v158 offset:6144
	v_mfma_f32_16x16x32_f16 v[74:77], v[146:149], v[118:121], v[74:77]
	ds_read_b128 v[102:105], v158 offset:8192
	v_mfma_f32_16x16x32_f16 v[18:21], v[150:153], v[118:121], v[18:21]
	ds_read_b128 v[106:109], v158 offset:10240
	v_mfma_f32_16x16x32_f16 v[26:29], v[154:157], v[118:121], v[26:29]
	s_add_u32 m0, s11, 0x19f00
	ds_read_b128 v[110:113], v160
	global_load_lds_dwordx4 v[222:223], off offset:256
	v_mfma_f32_16x16x32_f16 v[70:73], v[146:149], v[122:125], v[70:73]
	ds_read_b128 v[114:117], v160 offset:2048
	v_mfma_f32_16x16x32_f16 v[46:49], v[150:153], v[122:125], v[46:49]
	v_mfma_f32_16x16x32_f16 v[240:243], v[154:157], v[122:125], v[240:243]
	ds_read_b128 v[118:121], v160 offset:4096
	v_mfma_f32_16x16x32_f16 v[66:69], v[146:149], v[126:129], v[66:69]
	ds_read_b128 v[122:125], v160 offset:6144
	v_mfma_f32_16x16x32_f16 v[42:45], v[150:153], v[126:129], v[42:45]
	v_mfma_f32_16x16x32_f16 v[236:239], v[154:157], v[126:129], v[236:239]
	s_add_u32 m0, s11, 0x1bf00
	ds_read_b128 v[126:129], v160 offset:8192
	global_load_lds_dwordx4 v[226:227], off offset:256
	v_mfma_f32_16x16x32_f16 v[62:65], v[146:149], v[130:133], v[62:65]
	v_mfma_f32_16x16x32_f16 v[38:41], v[150:153], v[130:133], v[38:41]
	v_mfma_f32_16x16x32_f16 v[34:37], v[154:157], v[130:133], v[34:37]
	ds_read_b128 v[130:133], v160 offset:10240
	ds_read_b128 v[146:149], v164
	ds_read_b128 v[150:153], v164 offset:2048
	ds_read_b128 v[154:157], v164 offset:4096
	v_lshl_add_u64 v[218:219], v[218:219], 0, s[20:21]
	v_lshl_add_u64 v[222:223], v[222:223], 0, s[20:21]
	v_lshl_add_u64 v[226:227], v[226:227], 0, s[20:21]
	v_lshl_add_u64 v[220:221], v[220:221], 0, s[20:21]
	v_lshl_add_u64 v[224:225], v[224:225], 0, s[20:21]
	v_lshl_add_u64 v[228:229], v[228:229], 0, s[20:21]
	s_sub_u32 s22, s22, 1
	s_cmp_lg_u32 s22, 0
	s_cbranch_scc1 .Lgemm_Th_loop
	s_waitcnt lgkmcnt(9)
	v_mfma_f32_16x16x32_f16 v[82:85], v[134:137], v[86:89], v[82:85]
	v_mfma_f32_16x16x32_f16 v[58:61], v[138:141], v[86:89], v[58:61]
	v_mfma_f32_16x16x32_f16 v[14:17], v[142:145], v[86:89], v[14:17]
	s_add_u32 m0, s11, 0x1e080
	v_mfma_f32_16x16x32_f16 v[78:81], v[134:137], v[90:93], v[78:81]
	global_load_lds_dwordx4 v[220:221], off offset:-128
	v_mfma_f32_16x16x32_f16 v[22:25], v[138:141], v[90:93], v[22:25]
	v_mfma_f32_16x16x32_f16 v[30:33], v[142:145], v[90:93], v[30:33]
	v_mfma_f32_16x16x32_f16 v[74:77], v[134:137], v[94:97], v[74:77]
	v_mfma_f32_16x16x32_f16 v[18:21], v[138:141], v[94:97], v[18:21]
	v_mfma_f32_16x16x32_f16 v[26:29], v[142:145], v[94:97], v[26:29]
	s_add_u32 m0, s11, 0x20080
	v_mfma_f32_16x16x32_f16 v[70:73], v[134:137], v[98:101], v[70:73]
	global_load_lds_dwordx4 v[224:225], off offset:-128
	v_mfma_f32_16x16x32_f16 v[46:49], v[138:141], v[98:101], v[46:49]
	v_mfma_f32_16x16x32_f16 v[240:243], v[142:145], v[98:101], v[240:243]
	v_mfma_f32_16x16x32_f16 v[66:69], v[134:137], v[102:105], v[66:69]
	v_mfma_f32_16x16x32_f16 v[42:45], v[138:141], v[102:105], v[42:45]
	v_mfma_f32_16x16x32_f16 v[236:239], v[142:145], v[102:105], v[236:239]
	s_add_u32 m0, s11, 0x22080
	v_mfma_f32_16x16x32_f16 v[62:65], v[134:137], v[106:109], v[62:65]
	global_load_lds_dwordx4 v[228:229], off offset:-128
	v_mfma_f32_16x16x32_f16 v[38:41], v[138:141], v[106:109], v[38:41]
	v_mfma_f32_16x16x32_f16 v[34:37], v[142:145], v[106:109], v[34:37]
	s_waitcnt vmcnt(6) lgkmcnt(0)
	s_barrier
	ds_read_b128 v[134:137], v162 offset:49152
	v_mfma_f32_16x16x32_f16 v[82:85], v[146:149], v[110:113], v[82:85]
	ds_read_b128 v[138:141], v162 offset:51200
	v_mfma_f32_16x16x32_f16 v[58:61], v[150:153], v[110:113], v[58:61]
	ds_read_b128 v[142:145], v162 offset:53248
	v_mfma_f32_16x16x32_f16 v[14:17], v[154:157], v[110:113], v[14:17]
	s_add_u32 m0, s11, 0x0
	ds_read_b128 v[86:89], v158 offset:49152
	global_load_lds_dwordx4 v[218:219], off
	v_mfma_f32_16x16x32_f16 v[78:81], v[146:149], v[114:117], v[78:81]
	ds_read_b128 v[90:93], v158 offset:51200
	v_mfma_f32_16x16x32_f16 v[22:25], v[150:153], v[114:117], v[22:25]
	ds_read_b128 v[94:97], v158 offset:53248
	v_mfma_f32_16x16x32_f16 v[30:33], v[154:157], v[114:117], v[30:33]
	ds_read_b128 v[98:101], v158 offset:55296
	v_mfma_f32_16x16x32_f16 v[74:77], v[146:149], v[118:121], v[74:77]
	ds_read_b128 v[102:105], v158 offset:57344
	v_mfma_f32_16x16x32_f16 v[18:21], v[150:153], v[118:121], v[18:21]
	ds_read_b128 v[106:109], v158 offset:59392
	v_mfma_f32_16x16x32_f16 v[26:29], v[154:157], v[118:121], v[26:29]
	s_add_u32 m0, s11, 0x2000
	ds_read_b128 v[110:113], v160 offset:49152
	global_load_lds_dwordx4 v[222:223], off
	v_mfma_f32_16x16x32_f16 v[70:73], v[146:149], v[122:125], v[70:73]
	ds_read_b128 v[114:117], v160 offset:51200
	v_mfma_f32_16x16x32_f16 v[46:49], v[150:153], v[122:125], v[46:49]
	v_mfma_f32_16x16x32_f16 v[240:243], v[154:157], v[122:125], v[240:243]
	ds_read_b128 v[118:121], v160 offset:53248
	v_mfma_f32_16x16x32_f16 v[66:69], v[146:149], v[126:129], v[66:69]
	ds_read_b128 v[122:125], v160 offset:55296
	v_mfma_f32_16x16x32_f16 v[42:45], v[150:153], v[126:129], v[42:45]
	v_mfma_f32_16x16x32_f16 v[236:239], v[154:157], v[126:129], v[236:239]
	s_add_u32 m0, s11, 0x4000
	ds_read_b128 v[126:129], v160 offset:57344
	global_load_lds_dwordx4 v[226:227], off
	v_mfma_f32_16x16x32_f16 v[62:65], v[146:149], v[130:133], v[62:65]
	v_mfma_f32_16x16x32_f16 v[38:41], v[150:153], v[130:133], v[38:41]
	v_mfma_f32_16x16x32_f16 v[34:37], v[154:157], v[130:133], v[34:37]
	ds_read_b128 v[130:133], v160 offset:59392
	ds_read_b128 v[146:149], v164 offset:49152
	ds_read_b128 v[150:153], v164 offset:51200
	ds_read_b128 v[154:157], v164 offset:53248
	s_waitcnt lgkmcnt(9)
	v_mfma_f32_16x16x32_f16 v[82:85], v[134:137], v[86:89], v[82:85]
	v_mfma_f32_16x16x32_f16 v[58:61], v[138:141], v[86:89], v[58:61]
	v_mfma_f32_16x16x32_f16 v[14:17], v[142:145], v[86:89], v[14:17]
	s_add_u32 m0, s11, 0x6000
	v_mfma_f32_16x16x32_f16 v[78:81], v[134:137], v[90:93], v[78:81]
	global_load_lds_dwordx4 v[220:221], off
	v_mfma_f32_16x16x32_f16 v[22:25], v[138:141], v[90:93], v[22:25]
	v_mfma_f32_16x16x32_f16 v[30:33], v[142:145], v[90:93], v[30:33]
	v_mfma_f32_16x16x32_f16 v[74:77], v[134:137], v[94:97], v[74:77]
	v_mfma_f32_16x16x32_f16 v[18:21], v[138:141], v[94:97], v[18:21]
	v_mfma_f32_16x16x32_f16 v[26:29], v[142:145], v[94:97], v[26:29]
	s_add_u32 m0, s11, 0x8000
	v_mfma_f32_16x16x32_f16 v[70:73], v[134:137], v[98:101], v[70:73]
	global_load_lds_dwordx4 v[224:225], off
	v_mfma_f32_16x16x32_f16 v[46:49], v[138:141], v[98:101], v[46:49]
	v_mfma_f32_16x16x32_f16 v[240:243], v[142:145], v[98:101], v[240:243]
	v_mfma_f32_16x16x32_f16 v[66:69], v[134:137], v[102:105], v[66:69]
	v_mfma_f32_16x16x32_f16 v[42:45], v[138:141], v[102:105], v[42:45]
	v_mfma_f32_16x16x32_f16 v[236:239], v[142:145], v[102:105], v[236:239]
	s_add_u32 m0, s11, 0xa000
	v_mfma_f32_16x16x32_f16 v[62:65], v[134:137], v[106:109], v[62:65]
	global_load_lds_dwordx4 v[228:229], off
	v_mfma_f32_16x16x32_f16 v[38:41], v[138:141], v[106:109], v[38:41]
	v_mfma_f32_16x16x32_f16 v[34:37], v[142:145], v[106:109], v[34:37]
	s_waitcnt vmcnt(6) lgkmcnt(0)
	s_barrier
	s_lshl_b32 s26, s17, 2
	s_add_u32 s26, s24, s26
	s_addc_u32 s27, s25, 0
	v_lshlrev_b32_e32 v50, 4, v231
	global_load_dwordx4 v[10:13], v50, s[26:27]
	global_load_dwordx4 v[6:9], v50, s[26:27] offset:64
	global_load_dwordx4 v[2:5], v50, s[26:27] offset:128
	ds_read_b128 v[134:137], v163
	v_mfma_f32_16x16x32_f16 v[82:85], v[146:149], v[110:113], v[82:85]
	ds_read_b128 v[138:141], v163 offset:2048
	v_mfma_f32_16x16x32_f16 v[58:61], v[150:153], v[110:113], v[58:61]
	ds_read_b128 v[142:145], v163 offset:4096
	v_mfma_f32_16x16x32_f16 v[14:17], v[154:157], v[110:113], v[14:17]
	ds_read_b128 v[86:89], v159
	v_mfma_f32_16x16x32_f16 v[78:81], v[146:149], v[114:117], v[78:81]
	ds_read_b128 v[90:93], v159 offset:2048
	v_mfma_f32_16x16x32_f16 v[22:25], v[150:153], v[114:117], v[22:25]
	ds_read_b128 v[94:97], v159 offset:4096
	v_mfma_f32_16x16x32_f16 v[30:33], v[154:157], v[114:117], v[30:33]
	ds_read_b128 v[98:101], v159 offset:6144
	v_mfma_f32_16x16x32_f16 v[74:77], v[146:149], v[118:121], v[74:77]
	ds_read_b128 v[102:105], v159 offset:8192
	v_mfma_f32_16x16x32_f16 v[18:21], v[150:153], v[118:121], v[18:21]
	ds_read_b128 v[106:109], v159 offset:10240
	v_mfma_f32_16x16x32_f16 v[26:29], v[154:157], v[118:121], v[26:29]
	ds_read_b128 v[110:113], v161
	v_mfma_f32_16x16x32_f16 v[70:73], v[146:149], v[122:125], v[70:73]
	ds_read_b128 v[114:117], v161 offset:2048
	v_mfma_f32_16x16x32_f16 v[46:49], v[150:153], v[122:125], v[46:49]
	v_mfma_f32_16x16x32_f16 v[240:243], v[154:157], v[122:125], v[240:243]
	ds_read_b128 v[118:121], v161 offset:4096
	v_mfma_f32_16x16x32_f16 v[66:69], v[146:149], v[126:129], v[66:69]
	ds_read_b128 v[122:125], v161 offset:6144
	v_mfma_f32_16x16x32_f16 v[42:45], v[150:153], v[126:129], v[42:45]
	v_mfma_f32_16x16x32_f16 v[236:239], v[154:157], v[126:129], v[236:239]
	ds_read_b128 v[126:129], v161 offset:8192
	v_mfma_f32_16x16x32_f16 v[62:65], v[146:149], v[130:133], v[62:65]
	v_mfma_f32_16x16x32_f16 v[38:41], v[150:153], v[130:133], v[38:41]
	v_mfma_f32_16x16x32_f16 v[34:37], v[154:157], v[130:133], v[34:37]
	ds_read_b128 v[130:133], v161 offset:10240
	ds_read_b128 v[146:149], v165
	ds_read_b128 v[150:153], v165 offset:2048
	ds_read_b128 v[154:157], v165 offset:4096
	s_waitcnt lgkmcnt(9)
	v_mfma_f32_16x16x32_f16 v[82:85], v[134:137], v[86:89], v[82:85]
	v_mfma_f32_16x16x32_f16 v[58:61], v[138:141], v[86:89], v[58:61]
	v_mfma_f32_16x16x32_f16 v[14:17], v[142:145], v[86:89], v[14:17]
	v_mfma_f32_16x16x32_f16 v[78:81], v[134:137], v[90:93], v[78:81]
	v_mfma_f32_16x16x32_f16 v[22:25], v[138:141], v[90:93], v[22:25]
	v_mfma_f32_16x16x32_f16 v[30:33], v[142:145], v[90:93], v[30:33]
	v_mfma_f32_16x16x32_f16 v[74:77], v[134:137], v[94:97], v[74:77]
	v_mfma_f32_16x16x32_f16 v[18:21], v[138:141], v[94:97], v[18:21]
	v_mfma_f32_16x16x32_f16 v[26:29], v[142:145], v[94:97], v[26:29]
	v_mfma_f32_16x16x32_f16 v[70:73], v[134:137], v[98:101], v[70:73]
	v_mfma_f32_16x16x32_f16 v[46:49], v[138:141], v[98:101], v[46:49]
	v_mfma_f32_16x16x32_f16 v[240:243], v[142:145], v[98:101], v[240:243]
	v_mfma_f32_16x16x32_f16 v[66:69], v[134:137], v[102:105], v[66:69]
	v_mfma_f32_16x16x32_f16 v[42:45], v[138:141], v[102:105], v[42:45]
	v_mfma_f32_16x16x32_f16 v[236:239], v[142:145], v[102:105], v[236:239]
	v_mfma_f32_16x16x32_f16 v[62:65], v[134:137], v[106:109], v[62:65]
	v_mfma_f32_16x16x32_f16 v[38:41], v[138:141], v[106:109], v[38:41]
	v_mfma_f32_16x16x32_f16 v[34:37], v[142:145], v[106:109], v[34:37]
	s_waitcnt vmcnt(3) lgkmcnt(0)
	s_barrier
	ds_read_b128 v[134:137], v162
	v_mfma_f32_16x16x32_f16 v[82:85], v[146:149], v[110:113], v[82:85]
	ds_read_b128 v[138:141], v162 offset:2048
	v_mfma_f32_16x16x32_f16 v[58:61], v[150:153], v[110:113], v[58:61]
	ds_read_b128 v[142:145], v162 offset:4096
	v_mfma_f32_16x16x32_f16 v[14:17], v[154:157], v[110:113], v[14:17]
	ds_read_b128 v[86:89], v158
	v_mfma_f32_16x16x32_f16 v[78:81], v[146:149], v[114:117], v[78:81]
	ds_read_b128 v[90:93], v158 offset:2048
	v_mfma_f32_16x16x32_f16 v[22:25], v[150:153], v[114:117], v[22:25]
	ds_read_b128 v[94:97], v158 offset:4096
	v_mfma_f32_16x16x32_f16 v[30:33], v[154:157], v[114:117], v[30:33]
	ds_read_b128 v[98:101], v158 offset:6144
	v_mfma_f32_16x16x32_f16 v[74:77], v[146:149], v[118:121], v[74:77]
	ds_read_b128 v[102:105], v158 offset:8192
	v_mfma_f32_16x16x32_f16 v[18:21], v[150:153], v[118:121], v[18:21]
	ds_read_b128 v[106:109], v158 offset:10240
	v_mfma_f32_16x16x32_f16 v[26:29], v[154:157], v[118:121], v[26:29]
	ds_read_b128 v[110:113], v160
	v_mfma_f32_16x16x32_f16 v[70:73], v[146:149], v[122:125], v[70:73]
	ds_read_b128 v[114:117], v160 offset:2048
	v_mfma_f32_16x16x32_f16 v[46:49], v[150:153], v[122:125], v[46:49]
	v_mfma_f32_16x16x32_f16 v[240:243], v[154:157], v[122:125], v[240:243]
	ds_read_b128 v[118:121], v160 offset:4096
	v_mfma_f32_16x16x32_f16 v[66:69], v[146:149], v[126:129], v[66:69]
	ds_read_b128 v[122:125], v160 offset:6144
	v_mfma_f32_16x16x32_f16 v[42:45], v[150:153], v[126:129], v[42:45]
	v_mfma_f32_16x16x32_f16 v[236:239], v[154:157], v[126:129], v[236:239]
	ds_read_b128 v[126:129], v160 offset:8192
	v_mfma_f32_16x16x32_f16 v[62:65], v[146:149], v[130:133], v[62:65]
	v_mfma_f32_16x16x32_f16 v[38:41], v[150:153], v[130:133], v[38:41]
	v_mfma_f32_16x16x32_f16 v[34:37], v[154:157], v[130:133], v[34:37]
	ds_read_b128 v[130:133], v160 offset:10240
	ds_read_b128 v[146:149], v164
	ds_read_b128 v[150:153], v164 offset:2048
	ds_read_b128 v[154:157], v164 offset:4096
	s_waitcnt lgkmcnt(9)
	v_mfma_f32_16x16x32_f16 v[82:85], v[134:137], v[86:89], v[82:85]
	v_mfma_f32_16x16x32_f16 v[58:61], v[138:141], v[86:89], v[58:61]
	v_mfma_f32_16x16x32_f16 v[14:17], v[142:145], v[86:89], v[14:17]
	v_mfma_f32_16x16x32_f16 v[78:81], v[134:137], v[90:93], v[78:81]
	v_mfma_f32_16x16x32_f16 v[22:25], v[138:141], v[90:93], v[22:25]
	v_mfma_f32_16x16x32_f16 v[30:33], v[142:145], v[90:93], v[30:33]
	v_mfma_f32_16x16x32_f16 v[74:77], v[134:137], v[94:97], v[74:77]
	v_mfma_f32_16x16x32_f16 v[18:21], v[138:141], v[94:97], v[18:21]
	v_mfma_f32_16x16x32_f16 v[26:29], v[142:145], v[94:97], v[26:29]
	v_mfma_f32_16x16x32_f16 v[70:73], v[134:137], v[98:101], v[70:73]
	v_mfma_f32_16x16x32_f16 v[46:49], v[138:141], v[98:101], v[46:49]
	v_mfma_f32_16x16x32_f16 v[240:243], v[142:145], v[98:101], v[240:243]
	v_mfma_f32_16x16x32_f16 v[66:69], v[134:137], v[102:105], v[66:69]
	v_mfma_f32_16x16x32_f16 v[42:45], v[138:141], v[102:105], v[42:45]
	v_mfma_f32_16x16x32_f16 v[236:239], v[142:145], v[102:105], v[236:239]
	v_mfma_f32_16x16x32_f16 v[62:65], v[134:137], v[106:109], v[62:65]
	v_mfma_f32_16x16x32_f16 v[38:41], v[138:141], v[106:109], v[38:41]
	v_mfma_f32_16x16x32_f16 v[34:37], v[142:145], v[106:109], v[34:37]
	s_waitcnt lgkmcnt(0)
	v_mfma_f32_16x16x32_f16 v[82:85], v[146:149], v[110:113], v[82:85]
	v_mfma_f32_16x16x32_f16 v[58:61], v[150:153], v[110:113], v[58:61]
	v_mfma_f32_16x16x32_f16 v[14:17], v[154:157], v[110:113], v[14:17]
	v_mfma_f32_16x16x32_f16 v[78:81], v[146:149], v[114:117], v[78:81]
	v_mfma_f32_16x16x32_f16 v[22:25], v[150:153], v[114:117], v[22:25]
	v_mfma_f32_16x16x32_f16 v[30:33], v[154:157], v[114:117], v[30:33]
	v_mfma_f32_16x16x32_f16 v[74:77], v[146:149], v[118:121], v[74:77]
	v_mfma_f32_16x16x32_f16 v[18:21], v[150:153], v[118:121], v[18:21]
	v_mfma_f32_16x16x32_f16 v[26:29], v[154:157], v[118:121], v[26:29]
	v_mfma_f32_16x16x32_f16 v[70:73], v[146:149], v[122:125], v[70:73]
	v_mfma_f32_16x16x32_f16 v[46:49], v[150:153], v[122:125], v[46:49]
	v_mfma_f32_16x16x32_f16 v[240:243], v[154:157], v[122:125], v[240:243]
	v_mfma_f32_16x16x32_f16 v[66:69], v[146:149], v[126:129], v[66:69]
	v_mfma_f32_16x16x32_f16 v[42:45], v[150:153], v[126:129], v[42:45]
	v_mfma_f32_16x16x32_f16 v[236:239], v[154:157], v[126:129], v[236:239]
	v_mfma_f32_16x16x32_f16 v[62:65], v[146:149], v[130:133], v[62:65]
	v_mfma_f32_16x16x32_f16 v[38:41], v[150:153], v[130:133], v[38:41]
	v_mfma_f32_16x16x32_f16 v[34:37], v[154:157], v[130:133], v[34:37]
	s_branch .LBB1_76
.Lgemm_N_entry:
	s_cmp_lg_u32 s14, 0
	s_cbranch_scc1 .Lgemm_Nh_loop
.Lgemm_Nl_loop:
	s_waitcnt lgkmcnt(9)
	s_add_u32 m0, s11, 0x1e080
	v_mfma_f32_16x16x32_f16 v[82:85], v[86:89], v[134:137], v[82:85]
	global_load_lds_dwordx4 v[220:221], off offset:-128
	v_mfma_f32_16x16x32_f16 v[58:61], v[86:89], v[138:141], v[58:61]
	v_mfma_f32_16x16x32_f16 v[14:17], v[86:89], v[142:145], v[14:17]
	v_mfma_f32_16x16x32_f16 v[78:81], v[90:93], v[134:137], v[78:81]
	v_mfma_f32_16x16x32_f16 v[22:25], v[90:93], v[138:141], v[22:25]
	v_mfma_f32_16x16x32_f16 v[30:33], v[90:93], v[142:145], v[30:33]
	s_add_u32 m0, s11, 0x20080
	v_mfma_f32_16x16x32_f16 v[74:77], v[94:97], v[134:137], v[74:77]
	global_load_lds_dwordx4 v[224:225], off offset:-128
	v_mfma_f32_16x16x32_f16 v[18:21], v[94:97], v[138:141], v[18:21]
	v_mfma_f32_16x16x32_f16 v[26:29], v[94:97], v[142:145], v[26:29]
	v_mfma_f32_16x16x32_f16 v[70:73], v[98:101], v[134:137], v[70:73]
	v_mfma_f32_16x16x32_f16 v[46:49], v[98:101], v[138:141], v[46:49]
	v_mfma_f32_16x16x32_f16 v[240:243], v[98:101], v[142:145], v[240:243]
	s_add_u32 m0, s11, 0x22080
	v_mfma_f32_16x16x32_f16 v[66:69], v[102:105], v[134:137], v[66:69]
	global_load_lds_dwordx4 v[228:229], off offset:-128
	v_mfma_f32_16x16x32_f16 v[42:45], v[102:105], v[138:141], v[42:45]
	v_mfma_f32_16x16x32_f16 v[236:239], v[102:105], v[142:145], v[236:239]
	v_mfma_f32_16x16x32_f16 v[62:65], v[106:109], v[134:137], v[62:65]
	v_mfma_f32_16x16x32_f16 v[38:41], v[106:109], v[138:141], v[38:41]
	v_mfma_f32_16x16x32_f16 v[34:37], v[106:109], v[142:145], v[34:37]
	s_waitcnt vmcnt(6) lgkmcnt(0)
	s_barrier
	s_add_u32 m0, s11, 0x0
	ds_read_b128 v[134:137], v162 offset:49152
	global_load_lds_dwordx4 v[218:219], off
	v_mfma_f32_16x16x32_f16 v[82:85], v[110:113], v[146:149], v[82:85]
	ds_read_b128 v[138:141], v162 offset:51200
	v_mfma_f32_16x16x32_f16 v[58:61], v[110:113], v[150:153], v[58:61]
	ds_read_b128 v[142:145], v162 offset:53248
	v_mfma_f32_16x16x32_f16 v[14:17], v[110:113], v[154:157], v[14:17]
	ds_read_b128 v[86:89], v158 offset:49152
	v_mfma_f32_16x16x32_f16 v[78:81], v[114:117], v[146:149], v[78:81]
	ds_read_b128 v[90:93], v158 offset:51200
	v_mfma_f32_16x16x32_f16 v[22:25], v[114:117], v[150:153], v[22:25]
	ds_read_b128 v[94:97], v158 offset:53248
	v_mfma_f32_16x16x32_f16 v[30:33], v[114:117], v[154:157], v[30:33]
	s_add_u32 m0, s11, 0x2000
	ds_read_b128 v[98:101], v158 offset:55296
	global_load_lds_dwordx4 v[222:223], off
	v_mfma_f32_16x16x32_f16 v[74:77], v[118:121], v[146:149], v[74:77]
	ds_read_b128 v[102:105], v158 offset:57344
	v_mfma_f32_16x16x32_f16 v[18:21], v[118:121], v[150:153], v[18:21]
	ds_read_b128 v[106:109], v158 offset:59392
	v_mfma_f32_16x16x32_f16 v[26:29], v[118:121], v[154:157], v[26:29]
	ds_read_b128 v[110:113], v160 offset:49152
	v_mfma_f32_16x16x32_f16 v[70:73], v[122:125], v[146:149], v[70:73]
	ds_read_b128 v[114:117], v160 offset:51200
	v_mfma_f32_16x16x32_f16 v[46:49], v[122:125], v[150:153], v[46:49]
	v_mfma_f32_16x16x32_f16 v[240:243], v[122:125], v[154:157], v[240:243]
	s_add_u32 m0, s11, 0x4000
	ds_read_b128 v[118:121], v160 offset:53248
	global_load_lds_dwordx4 v[226:227], off
	v_mfma_f32_16x16x32_f16 v[66:69], v[126:129], v[146:149], v[66:69]
	ds_read_b128 v[122:125], v160 offset:55296
	v_mfma_f32_16x16x32_f16 v[42:45], v[126:129], v[150:153], v[42:45]
	v_mfma_f32_16x16x32_f16 v[236:239], v[126:129], v[154:157], v[236:239]
	ds_read_b128 v[126:129], v160 offset:57344
	v_mfma_f32_16x16x32_f16 v[62:65], v[130:133], v[146:149], v[62:65]
	v_mfma_f32_16x16x32_f16 v[38:41], v[130:133], v[150:153], v[38:41]
	v_mfma_f32_16x16x32_f16 v[34:37], v[130:133], v[154:157], v[34:37]
	ds_read_b128 v[130:133], v160 offset:59392
	ds_read_b128 v[146:149], v164 offset:49152
	ds_read_b128 v[150:153], v164 offset:51200
	ds_read_b128 v[154:157], v164 offset:53248
	s_waitcnt lgkmcnt(9)
	s_add_u32 m0, s11, 0x6000
	v_mfma_f32_16x16x32_f16 v[82:85], v[86:89], v[134:137], v[82:85]
	global_load_lds_dwordx4 v[220:221], off
	v_mfma_f32_16x16x32_f16 v[58:61], v[86:89], v[138:141], v[58:61]
	v_mfma_f32_16x16x32_f16 v[14:17], v[86:89], v[142:145], v[14:17]
	v_mfma_f32_16x16x32_f16 v[78:81], v[90:93], v[134:137], v[78:81]
	v_mfma_f32_16x16x32_f16 v[22:25], v[90:93], v[138:141], v[22:25]
	v_mfma_f32_16x16x32_f16 v[30:33], v[90:93], v[142:145], v[30:33]
	s_add_u32 m0, s11, 0x8000
	v_mfma_f32_16x16x32_f16 v[74:77], v[94:97], v[134:137], v[74:77]
	global_load_lds_dwordx4 v[224:225], off
	v_mfma_f32_16x16x32_f16 v[18:21], v[94:97], v[138:141], v[18:21]
	v_mfma_f32_16x16x32_f16 v[26:29], v[94:97], v[142:145], v[26:29]
	v_mfma_f32_16x16x32_f16 v[70:73], v[98:101], v[134:137], v[70:73]
	v_mfma_f32_16x16x32_f16 v[46:49], v[98:101], v[138:141], v[46:49]
	v_mfma_f32_16x16x32_f16 v[240:243], v[98:101], v[142:145], v[240:243]
	s_add_u32 m0, s11, 0xa000
	v_mfma_f32_16x16x32_f16 v[66:69], v[102:105], v[134:137], v[66:69]
	global_load_lds_dwordx4 v[228:229], off
	v_mfma_f32_16x16x32_f16 v[42:45], v[102:105], v[138:141], v[42:45]
	v_mfma_f32_16x16x32_f16 v[236:239], v[102:105], v[142:145], v[236:239]
	v_mfma_f32_16x16x32_f16 v[62:65], v[106:109], v[134:137], v[62:65]
	v_mfma_f32_16x16x32_f16 v[38:41], v[106:109], v[138:141], v[38:41]
	v_mfma_f32_16x16x32_f16 v[34:37], v[106:109], v[142:145], v[34:37]
	s_waitcnt vmcnt(6) lgkmcnt(0)
	s_barrier
	s_add_u32 m0, s11, 0xbf80
	ds_read_b128 v[134:137], v163
	global_load_lds_dwordx4 v[218:219], off offset:128
	v_mfma_f32_16x16x32_f16 v[82:85], v[110:113], v[146:149], v[82:85]
	ds_read_b128 v[138:141], v163 offset:2048
	v_mfma_f32_16x16x32_f16 v[58:61], v[110:113], v[150:153], v[58:61]
	ds_read_b128 v[142:145], v163 offset:4096
	v_mfma_f32_16x16x32_f16 v[14:17], v[110:113], v[154:157], v[14:17]
	ds_read_b128 v[86:89], v159
	v_mfma_f32_16x16x32_f16 v[78:81], v[114:117], v[146:149], v[78:81]
	ds_read_b128 v[90:93], v159 offset:2048
	v_mfma_f32_16x16x32_f16 v[22:25], v[114:117], v[150:153], v[22:25]
	ds_read_b128 v[94:97], v159 offset:4096
	v_mfma_f32_16x16x32_f16 v[30:33], v[114:117], v[154:157], v[30:33]
	s_add_u32 m0, s11, 0xdf80
	ds_read_b128 v[98:101], v159 offset:6144
	global_load_lds_dwordx4 v[222:223], off offset:128
	v_mfma_f32_16x16x32_f16 v[74:77], v[118:121], v[146:149], v[74:77]
	ds_read_b128 v[102:105], v159 offset:8192
	v_mfma_f32_16x16x32_f16 v[18:21], v[118:121], v[150:153], v[18:21]
	ds_read_b128 v[106:109], v159 offset:10240
	v_mfma_f32_16x16x32_f16 v[26:29], v[118:121], v[154:157], v[26:29]
	ds_read_b128 v[110:113], v161
	v_mfma_f32_16x16x32_f16 v[70:73], v[122:125], v[146:149], v[70:73]
	ds_read_b128 v[114:117], v161 offset:2048
	v_mfma_f32_16x16x32_f16 v[46:49], v[122:125], v[150:153], v[46:49]
	v_mfma_f32_16x16x32_f16 v[240:243], v[122:125], v[154:157], v[240:243]
	s_add_u32 m0, s11, 0xff80
	ds_read_b128 v[118:121], v161 offset:4096
	global_load_lds_dwordx4 v[226:227], off offset:128
	v_mfma_f32_16x16x32_f16 v[66:69], v[126:129], v[146:149], v[66:69]
	ds_read_b128 v[122:125], v161 offset:6144
	v_mfma_f32_16x16x32_f16 v[42:45], v[126:129], v[150:153], v[42:45]
	v_mfma_f32_16x16x32_f16 v[236:239], v[126:129], v[154:157], v[236:239]
	ds_read_b128 v[126:129], v161 offset:8192
	v_mfma_f32_16x16x32_f16 v[62:65], v[130:133], v[146:149], v[62:65]
	v_mfma_f32_16x16x32_f16 v[38:41], v[130:133], v[150:153], v[38:41]
	v_mfma_f32_16x16x32_f16 v[34:37], v[130:133], v[154:157], v[34:37]
	ds_read_b128 v[130:133], v161 offset:10240
	ds_read_b128 v[146:149], v165
	ds_read_b128 v[150:153], v165 offset:2048
	ds_read_b128 v[154:157], v165 offset:4096
	s_waitcnt lgkmcnt(9)
	s_add_u32 m0, s11, 0x11f80
	v_mfma_f32_16x16x32_f16 v[82:85], v[86:89], v[134:137], v[82:85]
	global_load_lds_dwordx4 v[220:221], off offset:128
	v_mfma_f32_16x16x32_f16 v[58:61], v[86:89], v[138:141], v[58:61]
	v_mfma_f32_16x16x32_f16 v[14:17], v[86:89], v[142:145], v[14:17]
	v_mfma_f32_16x16x32_f16 v[78:81], v[90:93], v[134:137], v[78:81]
	v_mfma_f32_16x16x32_f16 v[22:25], v[90:93], v[138:141], v[22:25]
	v_mfma_f32_16x16x32_f16 v[30:33], v[90:93], v[142:145], v[30:33]
	s_add_u32 m0, s11, 0x13f80
	v_mfma_f32_16x16x32_f16 v[74:77], v[94:97], v[134:137], v[74:77]
	global_load_lds_dwordx4 v[224:225], off offset:128
	v_mfma_f32_16x16x32_f16 v[18:21], v[94:97], v[138:141], v[18:21]
	v_mfma_f32_16x16x32_f16 v[26:29], v[94:97], v[142:145], v[26:29]
	v_mfma_f32_16x16x32_f16 v[70:73], v[98:101], v[134:137], v[70:73]
	v_mfma_f32_16x16x32_f16 v[46:49], v[98:101], v[138:141], v[46:49]
	v_mfma_f32_16x16x32_f16 v[240:243], v[98:101], v[142:145], v[240:243]
	s_add_u32 m0, s11, 0x15f80
	v_mfma_f32_16x16x32_f16 v[66:69], v[102:105], v[134:137], v[66:69]
	global_load_lds_dwordx4 v[228:229], off offset:128
	v_mfma_f32_16x16x32_f16 v[42:45], v[102:105], v[138:141], v[42:45]
	v_mfma_f32_16x16x32_f16 v[236:239], v[102:105], v[142:145], v[236:239]
	v_mfma_f32_16x16x32_f16 v[62:65], v[106:109], v[134:137], v[62:65]
	v_mfma_f32_16x16x32_f16 v[38:41], v[106:109], v[138:141], v[38:41]
	v_mfma_f32_16x16x32_f16 v[34:37], v[106:109], v[142:145], v[34:37]
	s_waitcnt vmcnt(6) lgkmcnt(0)
	s_barrier
	s_add_u32 m0, s11, 0x17f00
	ds_read_b128 v[134:137], v162
	global_load_lds_dwordx4 v[218:219], off offset:256
	v_mfma_f32_16x16x32_f16 v[82:85], v[110:113], v[146:149], v[82:85]
	ds_read_b128 v[138:141], v162 offset:2048
	v_mfma_f32_16x16x32_f16 v[58:61], v[110:113], v[150:153], v[58:61]
	ds_read_b128 v[142:145], v162 offset:4096
	v_mfma_f32_16x16x32_f16 v[14:17], v[110:113], v[154:157], v[14:17]
	ds_read_b128 v[86:89], v158
	v_mfma_f32_16x16x32_f16 v[78:81], v[114:117], v[146:149], v[78:81]
	ds_read_b128 v[90:93], v158 offset:2048
	v_mfma_f32_16x16x32_f16 v[22:25], v[114:117], v[150:153], v[22:25]
	ds_read_b128 v[94:97], v158 offset:4096
	v_mfma_f32_16x16x32_f16 v[30:33], v[114:117], v[154:157], v[30:33]
	s_add_u32 m0, s11, 0x19f00
	ds_read_b128 v[98:101], v158 offset:6144
	global_load_lds_dwordx4 v[222:223], off offset:256
	v_mfma_f32_16x16x32_f16 v[74:77], v[118:121], v[146:149], v[74:77]
	ds_read_b128 v[102:105], v158 offset:8192
	v_mfma_f32_16x16x32_f16 v[18:21], v[118:121], v[150:153], v[18:21]
	ds_read_b128 v[106:109], v158 offset:10240
	v_mfma_f32_16x16x32_f16 v[26:29], v[118:121], v[154:157], v[26:29]
	ds_read_b128 v[110:113], v160
	v_mfma_f32_16x16x32_f16 v[70:73], v[122:125], v[146:149], v[70:73]
	ds_read_b128 v[114:117], v160 offset:2048
	v_mfma_f32_16x16x32_f16 v[46:49], v[122:125], v[150:153], v[46:49]
	v_mfma_f32_16x16x32_f16 v[240:243], v[122:125], v[154:157], v[240:243]
	s_add_u32 m0, s11, 0x1bf00
	ds_read_b128 v[118:121], v160 offset:4096
	global_load_lds_dwordx4 v[226:227], off offset:256
	v_mfma_f32_16x16x32_f16 v[66:69], v[126:129], v[146:149], v[66:69]
	ds_read_b128 v[122:125], v160 offset:6144
	v_mfma_f32_16x16x32_f16 v[42:45], v[126:129], v[150:153], v[42:45]
	v_mfma_f32_16x16x32_f16 v[236:239], v[126:129], v[154:157], v[236:239]
	ds_read_b128 v[126:129], v160 offset:8192
	v_mfma_f32_16x16x32_f16 v[62:65], v[130:133], v[146:149], v[62:65]
	v_mfma_f32_16x16x32_f16 v[38:41], v[130:133], v[150:153], v[38:41]
	v_mfma_f32_16x16x32_f16 v[34:37], v[130:133], v[154:157], v[34:37]
	ds_read_b128 v[130:133], v160 offset:10240
	ds_read_b128 v[146:149], v164
	ds_read_b128 v[150:153], v164 offset:2048
	ds_read_b128 v[154:157], v164 offset:4096
	v_lshl_add_u64 v[218:219], v[218:219], 0, s[20:21]
	v_lshl_add_u64 v[222:223], v[222:223], 0, s[20:21]
	v_lshl_add_u64 v[226:227], v[226:227], 0, s[20:21]
	v_lshl_add_u64 v[220:221], v[220:221], 0, s[20:21]
	v_lshl_add_u64 v[224:225], v[224:225], 0, s[20:21]
	v_lshl_add_u64 v[228:229], v[228:229], 0, s[20:21]
	s_sub_u32 s22, s22, 1
	s_cmp_lg_u32 s22, 0
	s_cbranch_scc1 .Lgemm_Nl_loop
	s_waitcnt lgkmcnt(9)
	s_add_u32 m0, s11, 0x1e080
	v_mfma_f32_16x16x32_f16 v[82:85], v[86:89], v[134:137], v[82:85]
	global_load_lds_dwordx4 v[220:221], off offset:-128
	v_mfma_f32_16x16x32_f16 v[58:61], v[86:89], v[138:141], v[58:61]
	v_mfma_f32_16x16x32_f16 v[14:17], v[86:89], v[142:145], v[14:17]
	v_mfma_f32_16x16x32_f16 v[78:81], v[90:93], v[134:137], v[78:81]
	v_mfma_f32_16x16x32_f16 v[22:25], v[90:93], v[138:141], v[22:25]
	v_mfma_f32_16x16x32_f16 v[30:33], v[90:93], v[142:145], v[30:33]
	s_add_u32 m0, s11, 0x20080
	v_mfma_f32_16x16x32_f16 v[74:77], v[94:97], v[134:137], v[74:77]
	global_load_lds_dwordx4 v[224:225], off offset:-128
	v_mfma_f32_16x16x32_f16 v[18:21], v[94:97], v[138:141], v[18:21]
	v_mfma_f32_16x16x32_f16 v[26:29], v[94:97], v[142:145], v[26:29]
	v_mfma_f32_16x16x32_f16 v[70:73], v[98:101], v[134:137], v[70:73]
	v_mfma_f32_16x16x32_f16 v[46:49], v[98:101], v[138:141], v[46:49]
	v_mfma_f32_16x16x32_f16 v[240:243], v[98:101], v[142:145], v[240:243]
	s_add_u32 m0, s11, 0x22080
	v_mfma_f32_16x16x32_f16 v[66:69], v[102:105], v[134:137], v[66:69]
	global_load_lds_dwordx4 v[228:229], off offset:-128
	v_mfma_f32_16x16x32_f16 v[42:45], v[102:105], v[138:141], v[42:45]
	v_mfma_f32_16x16x32_f16 v[236:239], v[102:105], v[142:145], v[236:239]
	v_mfma_f32_16x16x32_f16 v[62:65], v[106:109], v[134:137], v[62:65]
	v_mfma_f32_16x16x32_f16 v[38:41], v[106:109], v[138:141], v[38:41]
	v_mfma_f32_16x16x32_f16 v[34:37], v[106:109], v[142:145], v[34:37]
	s_waitcnt vmcnt(6) lgkmcnt(0)
	s_barrier
	s_add_u32 m0, s11, 0x0
	ds_read_b128 v[134:137], v162 offset:49152
	global_load_lds_dwordx4 v[218:219], off
	v_mfma_f32_16x16x32_f16 v[82:85], v[110:113], v[146:149], v[82:85]
	ds_read_b128 v[138:141], v162 offset:51200
	v_mfma_f32_16x16x32_f16 v[58:61], v[110:113], v[150:153], v[58:61]
	ds_read_b128 v[142:145], v162 offset:53248
	v_mfma_f32_16x16x32_f16 v[14:17], v[110:113], v[154:157], v[14:17]
	ds_read_b128 v[86:89], v158 offset:49152
	v_mfma_f32_16x16x32_f16 v[78:81], v[114:117], v[146:149], v[78:81]
	ds_read_b128 v[90:93], v158 offset:51200
	v_mfma_f32_16x16x32_f16 v[22:25], v[114:117], v[150:153], v[22:25]
	ds_read_b128 v[94:97], v158 offset:53248
	v_mfma_f32_16x16x32_f16 v[30:33], v[114:117], v[154:157], v[30:33]
	s_add_u32 m0, s11, 0x2000
	ds_read_b128 v[98:101], v158 offset:55296
	global_load_lds_dwordx4 v[222:223], off
	v_mfma_f32_16x16x32_f16 v[74:77], v[118:121], v[146:149], v[74:77]
	ds_read_b128 v[102:105], v158 offset:57344
	v_mfma_f32_16x16x32_f16 v[18:21], v[118:121], v[150:153], v[18:21]
	ds_read_b128 v[106:109], v158 offset:59392
	v_mfma_f32_16x16x32_f16 v[26:29], v[118:121], v[154:157], v[26:29]
	ds_read_b128 v[110:113], v160 offset:49152
	v_mfma_f32_16x16x32_f16 v[70:73], v[122:125], v[146:149], v[70:73]
	ds_read_b128 v[114:117], v160 offset:51200
	v_mfma_f32_16x16x32_f16 v[46:49], v[122:125], v[150:153], v[46:49]
	v_mfma_f32_16x16x32_f16 v[240:243], v[122:125], v[154:157], v[240:243]
	s_add_u32 m0, s11, 0x4000
	ds_read_b128 v[118:121], v160 offset:53248
	global_load_lds_dwordx4 v[226:227], off
	v_mfma_f32_16x16x32_f16 v[66:69], v[126:129], v[146:149], v[66:69]
	ds_read_b128 v[122:125], v160 offset:55296
	v_mfma_f32_16x16x32_f16 v[42:45], v[126:129], v[150:153], v[42:45]
	v_mfma_f32_16x16x32_f16 v[236:239], v[126:129], v[154:157], v[236:239]
	ds_read_b128 v[126:129], v160 offset:57344
	v_mfma_f32_16x16x32_f16 v[62:65], v[130:133], v[146:149], v[62:65]
	v_mfma_f32_16x16x32_f16 v[38:41], v[130:133], v[150:153], v[38:41]
	v_mfma_f32_16x16x32_f16 v[34:37], v[130:133], v[154:157], v[34:37]
	ds_read_b128 v[130:133], v160 offset:59392
	ds_read_b128 v[146:149], v164 offset:49152
	ds_read_b128 v[150:153], v164 offset:51200
	ds_read_b128 v[154:157], v164 offset:53248
	s_waitcnt lgkmcnt(9)
	s_add_u32 m0, s11, 0x6000
	v_mfma_f32_16x16x32_f16 v[82:85], v[86:89], v[134:137], v[82:85]
	global_load_lds_dwordx4 v[220:221], off
	v_mfma_f32_16x16x32_f16 v[58:61], v[86:89], v[138:141], v[58:61]
	v_mfma_f32_16x16x32_f16 v[14:17], v[86:89], v[142:145], v[14:17]
	v_mfma_f32_16x16x32_f16 v[78:81], v[90:93], v[134:137], v[78:81]
	v_mfma_f32_16x16x32_f16 v[22:25], v[90:93], v[138:141], v[22:25]
	v_mfma_f32_16x16x32_f16 v[30:33], v[90:93], v[142:145], v[30:33]
	s_add_u32 m0, s11, 0x8000
	v_mfma_f32_16x16x32_f16 v[74:77], v[94:97], v[134:137], v[74:77]
	global_load_lds_dwordx4 v[224:225], off
	v_mfma_f32_16x16x32_f16 v[18:21], v[94:97], v[138:141], v[18:21]
	v_mfma_f32_16x16x32_f16 v[26:29], v[94:97], v[142:145], v[26:29]
	v_mfma_f32_16x16x32_f16 v[70:73], v[98:101], v[134:137], v[70:73]
	v_mfma_f32_16x16x32_f16 v[46:49], v[98:101], v[138:141], v[46:49]
	v_mfma_f32_16x16x32_f16 v[240:243], v[98:101], v[142:145], v[240:243]
	s_add_u32 m0, s11, 0xa000
	v_mfma_f32_16x16x32_f16 v[66:69], v[102:105], v[134:137], v[66:69]
	global_load_lds_dwordx4 v[228:229], off
	v_mfma_f32_16x16x32_f16 v[42:45], v[102:105], v[138:141], v[42:45]
	v_mfma_f32_16x16x32_f16 v[236:239], v[102:105], v[142:145], v[236:239]
	v_mfma_f32_16x16x32_f16 v[62:65], v[106:109], v[134:137], v[62:65]
	v_mfma_f32_16x16x32_f16 v[38:41], v[106:109], v[138:141], v[38:41]
	v_mfma_f32_16x16x32_f16 v[34:37], v[106:109], v[142:145], v[34:37]
	s_waitcnt vmcnt(6) lgkmcnt(0)
	s_barrier
	s_lshl_b32 s26, s17, 2
	s_add_u32 s26, s24, s26
	s_addc_u32 s27, s25, 0
	v_lshlrev_b32_e32 v50, 2, v1
	global_load_dword v234, v50, s[26:27]
	global_load_dword v232, v50, s[26:27] offset:64
	global_load_dword v230, v50, s[26:27] offset:128
	ds_read_b128 v[134:137], v163
	v_mfma_f32_16x16x32_f16 v[82:85], v[110:113], v[146:149], v[82:85]
	ds_read_b128 v[138:141], v163 offset:2048
	v_mfma_f32_16x16x32_f16 v[58:61], v[110:113], v[150:153], v[58:61]
	ds_read_b128 v[142:145], v163 offset:4096
	v_mfma_f32_16x16x32_f16 v[14:17], v[110:113], v[154:157], v[14:17]
	ds_read_b128 v[86:89], v159
	v_mfma_f32_16x16x32_f16 v[78:81], v[114:117], v[146:149], v[78:81]
	ds_read_b128 v[90:93], v159 offset:2048
	v_mfma_f32_16x16x32_f16 v[22:25], v[114:117], v[150:153], v[22:25]
	ds_read_b128 v[94:97], v159 offset:4096
	v_mfma_f32_16x16x32_f16 v[30:33], v[114:117], v[154:157], v[30:33]
	ds_read_b128 v[98:101], v159 offset:6144
	v_mfma_f32_16x16x32_f16 v[74:77], v[118:121], v[146:149], v[74:77]
	ds_read_b128 v[102:105], v159 offset:8192
	v_mfma_f32_16x16x32_f16 v[18:21], v[118:121], v[150:153], v[18:21]
	ds_read_b128 v[106:109], v159 offset:10240
	v_mfma_f32_16x16x32_f16 v[26:29], v[118:121], v[154:157], v[26:29]
	ds_read_b128 v[110:113], v161
	v_mfma_f32_16x16x32_f16 v[70:73], v[122:125], v[146:149], v[70:73]
	ds_read_b128 v[114:117], v161 offset:2048
	v_mfma_f32_16x16x32_f16 v[46:49], v[122:125], v[150:153], v[46:49]
	v_mfma_f32_16x16x32_f16 v[240:243], v[122:125], v[154:157], v[240:243]
	ds_read_b128 v[118:121], v161 offset:4096
	v_mfma_f32_16x16x32_f16 v[66:69], v[126:129], v[146:149], v[66:69]
	ds_read_b128 v[122:125], v161 offset:6144
	v_mfma_f32_16x16x32_f16 v[42:45], v[126:129], v[150:153], v[42:45]
	v_mfma_f32_16x16x32_f16 v[236:239], v[126:129], v[154:157], v[236:239]
	ds_read_b128 v[126:129], v161 offset:8192
	v_mfma_f32_16x16x32_f16 v[62:65], v[130:133], v[146:149], v[62:65]
	v_mfma_f32_16x16x32_f16 v[38:41], v[130:133], v[150:153], v[38:41]
	v_mfma_f32_16x16x32_f16 v[34:37], v[130:133], v[154:157], v[34:37]
	ds_read_b128 v[130:133], v161 offset:10240
	ds_read_b128 v[146:149], v165
	ds_read_b128 v[150:153], v165 offset:2048
	ds_read_b128 v[154:157], v165 offset:4096
	s_waitcnt lgkmcnt(9)
	v_mfma_f32_16x16x32_f16 v[82:85], v[86:89], v[134:137], v[82:85]
	v_mfma_f32_16x16x32_f16 v[58:61], v[86:89], v[138:141], v[58:61]
	v_mfma_f32_16x16x32_f16 v[14:17], v[86:89], v[142:145], v[14:17]
	v_mfma_f32_16x16x32_f16 v[78:81], v[90:93], v[134:137], v[78:81]
	v_mfma_f32_16x16x32_f16 v[22:25], v[90:93], v[138:141], v[22:25]
	v_mfma_f32_16x16x32_f16 v[30:33], v[90:93], v[142:145], v[30:33]
	v_mfma_f32_16x16x32_f16 v[74:77], v[94:97], v[134:137], v[74:77]
	v_mfma_f32_16x16x32_f16 v[18:21], v[94:97], v[138:141], v[18:21]
	v_mfma_f32_16x16x32_f16 v[26:29], v[94:97], v[142:145], v[26:29]
	v_mfma_f32_16x16x32_f16 v[70:73], v[98:101], v[134:137], v[70:73]
	v_mfma_f32_16x16x32_f16 v[46:49], v[98:101], v[138:141], v[46:49]
	v_mfma_f32_16x16x32_f16 v[240:243], v[98:101], v[142:145], v[240:243]
	v_mfma_f32_16x16x32_f16 v[66:69], v[102:105], v[134:137], v[66:69]
	v_mfma_f32_16x16x32_f16 v[42:45], v[102:105], v[138:141], v[42:45]
	v_mfma_f32_16x16x32_f16 v[236:239], v[102:105], v[142:145], v[236:239]
	v_mfma_f32_16x16x32_f16 v[62:65], v[106:109], v[134:137], v[62:65]
	v_mfma_f32_16x16x32_f16 v[38:41], v[106:109], v[138:141], v[38:41]
	v_mfma_f32_16x16x32_f16 v[34:37], v[106:109], v[142:145], v[34:37]
	s_waitcnt vmcnt(3) lgkmcnt(0)
	s_barrier
	ds_read_b128 v[134:137], v162
	v_mfma_f32_16x16x32_f16 v[82:85], v[110:113], v[146:149], v[82:85]
	ds_read_b128 v[138:141], v162 offset:2048
	v_mfma_f32_16x16x32_f16 v[58:61], v[110:113], v[150:153], v[58:61]
	ds_read_b128 v[142:145], v162 offset:4096
	v_mfma_f32_16x16x32_f16 v[14:17], v[110:113], v[154:157], v[14:17]
	ds_read_b128 v[86:89], v158
	v_mfma_f32_16x16x32_f16 v[78:81], v[114:117], v[146:149], v[78:81]
	ds_read_b128 v[90:93], v158 offset:2048
	v_mfma_f32_16x16x32_f16 v[22:25], v[114:117], v[150:153], v[22:25]
	ds_read_b128 v[94:97], v158 offset:4096
	v_mfma_f32_16x16x32_f16 v[30:33], v[114:117], v[154:157], v[30:33]
	ds_read_b128 v[98:101], v158 offset:6144
	v_mfma_f32_16x16x32_f16 v[74:77], v[118:121], v[146:149], v[74:77]
	ds_read_b128 v[102:105], v158 offset:8192
	v_mfma_f32_16x16x32_f16 v[18:21], v[118:121], v[150:153], v[18:21]
	ds_read_b128 v[106:109], v158 offset:10240
	v_mfma_f32_16x16x32_f16 v[26:29], v[118:121], v[154:157], v[26:29]
	ds_read_b128 v[110:113], v160
	v_mfma_f32_16x16x32_f16 v[70:73], v[122:125], v[146:149], v[70:73]
	ds_read_b128 v[114:117], v160 offset:2048
	v_mfma_f32_16x16x32_f16 v[46:49], v[122:125], v[150:153], v[46:49]
	v_mfma_f32_16x16x32_f16 v[240:243], v[122:125], v[154:157], v[240:243]
	ds_read_b128 v[118:121], v160 offset:4096
	v_mfma_f32_16x16x32_f16 v[66:69], v[126:129], v[146:149], v[66:69]
	ds_read_b128 v[122:125], v160 offset:6144
	v_mfma_f32_16x16x32_f16 v[42:45], v[126:129], v[150:153], v[42:45]
	v_mfma_f32_16x16x32_f16 v[236:239], v[126:129], v[154:157], v[236:239]
	ds_read_b128 v[126:129], v160 offset:8192
	v_mfma_f32_16x16x32_f16 v[62:65], v[130:133], v[146:149], v[62:65]
	v_mfma_f32_16x16x32_f16 v[38:41], v[130:133], v[150:153], v[38:41]
	v_mfma_f32_16x16x32_f16 v[34:37], v[130:133], v[154:157], v[34:37]
	ds_read_b128 v[130:133], v160 offset:10240
	ds_read_b128 v[146:149], v164
	ds_read_b128 v[150:153], v164 offset:2048
	ds_read_b128 v[154:157], v164 offset:4096
	s_waitcnt lgkmcnt(9)
	v_mfma_f32_16x16x32_f16 v[82:85], v[86:89], v[134:137], v[82:85]
	v_mfma_f32_16x16x32_f16 v[58:61], v[86:89], v[138:141], v[58:61]
	v_mfma_f32_16x16x32_f16 v[14:17], v[86:89], v[142:145], v[14:17]
	v_mfma_f32_16x16x32_f16 v[78:81], v[90:93], v[134:137], v[78:81]
	v_mfma_f32_16x16x32_f16 v[22:25], v[90:93], v[138:141], v[22:25]
	v_mfma_f32_16x16x32_f16 v[30:33], v[90:93], v[142:145], v[30:33]
	v_mfma_f32_16x16x32_f16 v[74:77], v[94:97], v[134:137], v[74:77]
	v_mfma_f32_16x16x32_f16 v[18:21], v[94:97], v[138:141], v[18:21]
	v_mfma_f32_16x16x32_f16 v[26:29], v[94:97], v[142:145], v[26:29]
	v_mfma_f32_16x16x32_f16 v[70:73], v[98:101], v[134:137], v[70:73]
	v_mfma_f32_16x16x32_f16 v[46:49], v[98:101], v[138:141], v[46:49]
	v_mfma_f32_16x16x32_f16 v[240:243], v[98:101], v[142:145], v[240:243]
	v_mfma_f32_16x16x32_f16 v[66:69], v[102:105], v[134:137], v[66:69]
	v_mfma_f32_16x16x32_f16 v[42:45], v[102:105], v[138:141], v[42:45]
	v_mfma_f32_16x16x32_f16 v[236:239], v[102:105], v[142:145], v[236:239]
	v_mfma_f32_16x16x32_f16 v[62:65], v[106:109], v[134:137], v[62:65]
	v_mfma_f32_16x16x32_f16 v[38:41], v[106:109], v[138:141], v[38:41]
	v_mfma_f32_16x16x32_f16 v[34:37], v[106:109], v[142:145], v[34:37]
	s_waitcnt lgkmcnt(0)
	v_mfma_f32_16x16x32_f16 v[82:85], v[110:113], v[146:149], v[82:85]
	v_mfma_f32_16x16x32_f16 v[58:61], v[110:113], v[150:153], v[58:61]
	v_mfma_f32_16x16x32_f16 v[14:17], v[110:113], v[154:157], v[14:17]
	v_mfma_f32_16x16x32_f16 v[78:81], v[114:117], v[146:149], v[78:81]
	v_mfma_f32_16x16x32_f16 v[22:25], v[114:117], v[150:153], v[22:25]
	v_mfma_f32_16x16x32_f16 v[30:33], v[114:117], v[154:157], v[30:33]
	v_mfma_f32_16x16x32_f16 v[74:77], v[118:121], v[146:149], v[74:77]
	v_mfma_f32_16x16x32_f16 v[18:21], v[118:121], v[150:153], v[18:21]
	v_mfma_f32_16x16x32_f16 v[26:29], v[118:121], v[154:157], v[26:29]
	v_mfma_f32_16x16x32_f16 v[70:73], v[122:125], v[146:149], v[70:73]
	v_mfma_f32_16x16x32_f16 v[46:49], v[122:125], v[150:153], v[46:49]
	v_mfma_f32_16x16x32_f16 v[240:243], v[122:125], v[154:157], v[240:243]
	v_mfma_f32_16x16x32_f16 v[66:69], v[126:129], v[146:149], v[66:69]
	v_mfma_f32_16x16x32_f16 v[42:45], v[126:129], v[150:153], v[42:45]
	v_mfma_f32_16x16x32_f16 v[236:239], v[126:129], v[154:157], v[236:239]
	v_mfma_f32_16x16x32_f16 v[62:65], v[130:133], v[146:149], v[62:65]
	v_mfma_f32_16x16x32_f16 v[38:41], v[130:133], v[150:153], v[38:41]
	v_mfma_f32_16x16x32_f16 v[34:37], v[130:133], v[154:157], v[34:37]
	s_branch .LBB1_76
.Lgemm_Nh_loop:
	s_waitcnt lgkmcnt(9)
	v_mfma_f32_16x16x32_f16 v[82:85], v[86:89], v[134:137], v[82:85]
	v_mfma_f32_16x16x32_f16 v[58:61], v[86:89], v[138:141], v[58:61]
	v_mfma_f32_16x16x32_f16 v[14:17], v[86:89], v[142:145], v[14:17]
	s_add_u32 m0, s11, 0x1e080
	v_mfma_f32_16x16x32_f16 v[78:81], v[90:93], v[134:137], v[78:81]
	global_load_lds_dwordx4 v[220:221], off offset:-128
	v_mfma_f32_16x16x32_f16 v[22:25], v[90:93], v[138:141], v[22:25]
	v_mfma_f32_16x16x32_f16 v[30:33], v[90:93], v[142:145], v[30:33]
	v_mfma_f32_16x16x32_f16 v[74:77], v[94:97], v[134:137], v[74:77]
	v_mfma_f32_16x16x32_f16 v[18:21], v[94:97], v[138:141], v[18:21]
	v_mfma_f32_16x16x32_f16 v[26:29], v[94:97], v[142:145], v[26:29]
	s_add_u32 m0, s11, 0x20080
	v_mfma_f32_16x16x32_f16 v[70:73], v[98:101], v[134:137], v[70:73]
	global_load_lds_dwordx4 v[224:225], off offset:-128
	v_mfma_f32_16x16x32_f16 v[46:49], v[98:101], v[138:141], v[46:49]
	v_mfma_f32_16x16x32_f16 v[240:243], v[98:101], v[142:145], v[240:243]
	v_mfma_f32_16x16x32_f16 v[66:69], v[102:105], v[134:137], v[66:69]
	v_mfma_f32_16x16x32_f16 v[42:45], v[102:105], v[138:141], v[42:45]
	v_mfma_f32_16x16x32_f16 v[236:239], v[102:105], v[142:145], v[236:239]
	s_add_u32 m0, s11, 0x22080
	v_mfma_f32_16x16x32_f16 v[62:65], v[106:109], v[134:137], v[62:65]
	global_load_lds_dwordx4 v[228:229], off offset:-128
	v_mfma_f32_16x16x32_f16 v[38:41], v[106:109], v[138:141], v[38:41]
	v_mfma_f32_16x16x32_f16 v[34:37], v[106:109], v[142:145], v[34:37]
	s_waitcnt vmcnt(6) lgkmcnt(0)
	s_barrier
	ds_read_b128 v[134:137], v162 offset:49152
	v_mfma_f32_16x16x32_f16 v[82:85], v[110:113], v[146:149], v[82:85]
	ds_read_b128 v[138:141], v162 offset:51200
	v_mfma_f32_16x16x32_f16 v[58:61], v[110:113], v[150:153], v[58:61]
	ds_read_b128 v[142:145], v162 offset:53248
	v_mfma_f32_16x16x32_f16 v[14:17], v[110:113], v[154:157], v[14:17]
	s_add_u32 m0, s11, 0x0
	ds_read_b128 v[86:89], v158 offset:49152
	global_load_lds_dwordx4 v[218:219], off
	v_mfma_f32_16x16x32_f16 v[78:81], v[114:117], v[146:149], v[78:81]
	ds_read_b128 v[90:93], v158 offset:51200
	v_mfma_f32_16x16x32_f16 v[22:25], v[114:117], v[150:153], v[22:25]
	ds_read_b128 v[94:97], v158 offset:53248
	v_mfma_f32_16x16x32_f16 v[30:33], v[114:117], v[154:157], v[30:33]
	ds_read_b128 v[98:101], v158 offset:55296
	v_mfma_f32_16x16x32_f16 v[74:77], v[118:121], v[146:149], v[74:77]
	ds_read_b128 v[102:105], v158 offset:57344
	v_mfma_f32_16x16x32_f16 v[18:21], v[118:121], v[150:153], v[18:21]
	ds_read_b128 v[106:109], v158 offset:59392
	v_mfma_f32_16x16x32_f16 v[26:29], v[118:121], v[154:157], v[26:29]
	s_add_u32 m0, s11, 0x2000
	ds_read_b128 v[110:113], v160 offset:49152
	global_load_lds_dwordx4 v[222:223], off
	v_mfma_f32_16x16x32_f16 v[70:73], v[122:125], v[146:149], v[70:73]
	ds_read_b128 v[114:117], v160 offset:51200
	v_mfma_f32_16x16x32_f16 v[46:49], v[122:125], v[150:153], v[46:49]
	v_mfma_f32_16x16x32_f16 v[240:243], v[122:125], v[154:157], v[240:243]
	ds_read_b128 v[118:121], v160 offset:53248
	v_mfma_f32_16x16x32_f16 v[66:69], v[126:129], v[146:149], v[66:69]
	ds_read_b128 v[122:125], v160 offset:55296
	v_mfma_f32_16x16x32_f16 v[42:45], v[126:129], v[150:153], v[42:45]
	v_mfma_f32_16x16x32_f16 v[236:239], v[126:129], v[154:157], v[236:239]
	s_add_u32 m0, s11, 0x4000
	ds_read_b128 v[126:129], v160 offset:57344
	global_load_lds_dwordx4 v[226:227], off
	v_mfma_f32_16x16x32_f16 v[62:65], v[130:133], v[146:149], v[62:65]
	v_mfma_f32_16x16x32_f16 v[38:41], v[130:133], v[150:153], v[38:41]
	v_mfma_f32_16x16x32_f16 v[34:37], v[130:133], v[154:157], v[34:37]
	ds_read_b128 v[130:133], v160 offset:59392
	ds_read_b128 v[146:149], v164 offset:49152
	ds_read_b128 v[150:153], v164 offset:51200
	ds_read_b128 v[154:157], v164 offset:53248
	s_waitcnt lgkmcnt(9)
	v_mfma_f32_16x16x32_f16 v[82:85], v[86:89], v[134:137], v[82:85]
	v_mfma_f32_16x16x32_f16 v[58:61], v[86:89], v[138:141], v[58:61]
	v_mfma_f32_16x16x32_f16 v[14:17], v[86:89], v[142:145], v[14:17]
	s_add_u32 m0, s11, 0x6000
	v_mfma_f32_16x16x32_f16 v[78:81], v[90:93], v[134:137], v[78:81]
	global_load_lds_dwordx4 v[220:221], off
	v_mfma_f32_16x16x32_f16 v[22:25], v[90:93], v[138:141], v[22:25]
	v_mfma_f32_16x16x32_f16 v[30:33], v[90:93], v[142:145], v[30:33]
	v_mfma_f32_16x16x32_f16 v[74:77], v[94:97], v[134:137], v[74:77]
	v_mfma_f32_16x16x32_f16 v[18:21], v[94:97], v[138:141], v[18:21]
	v_mfma_f32_16x16x32_f16 v[26:29], v[94:97], v[142:145], v[26:29]
	s_add_u32 m0, s11, 0x8000
	v_mfma_f32_16x16x32_f16 v[70:73], v[98:101], v[134:137], v[70:73]
	global_load_lds_dwordx4 v[224:225], off
	v_mfma_f32_16x16x32_f16 v[46:49], v[98:101], v[138:141], v[46:49]
	v_mfma_f32_16x16x32_f16 v[240:243], v[98:101], v[142:145], v[240:243]
	v_mfma_f32_16x16x32_f16 v[66:69], v[102:105], v[134:137], v[66:69]
	v_mfma_f32_16x16x32_f16 v[42:45], v[102:105], v[138:141], v[42:45]
	v_mfma_f32_16x16x32_f16 v[236:239], v[102:105], v[142:145], v[236:239]
	s_add_u32 m0, s11, 0xa000
	v_mfma_f32_16x16x32_f16 v[62:65], v[106:109], v[134:137], v[62:65]
	global_load_lds_dwordx4 v[228:229], off
	v_mfma_f32_16x16x32_f16 v[38:41], v[106:109], v[138:141], v[38:41]
	v_mfma_f32_16x16x32_f16 v[34:37], v[106:109], v[142:145], v[34:37]
	s_waitcnt vmcnt(6) lgkmcnt(0)
	s_barrier
	ds_read_b128 v[134:137], v163
	v_mfma_f32_16x16x32_f16 v[82:85], v[110:113], v[146:149], v[82:85]
	ds_read_b128 v[138:141], v163 offset:2048
	v_mfma_f32_16x16x32_f16 v[58:61], v[110:113], v[150:153], v[58:61]
	ds_read_b128 v[142:145], v163 offset:4096
	v_mfma_f32_16x16x32_f16 v[14:17], v[110:113], v[154:157], v[14:17]
	s_add_u32 m0, s11, 0xbf80
	ds_read_b128 v[86:89], v159
	global_load_lds_dwordx4 v[218:219], off offset:128
	v_mfma_f32_16x16x32_f16 v[78:81], v[114:117], v[146:149], v[78:81]
	ds_read_b128 v[90:93], v159 offset:2048
	v_mfma_f32_16x16x32_f16 v[22:25], v[114:117], v[150:153], v[22:25]
	ds_read_b128 v[94:97], v159 offset:4096
	v_mfma_f32_16x16x32_f16 v[30:33], v[114:117], v[154:157], v[30:33]
	ds_read_b128 v[98:101], v159 offset:6144
	v_mfma_f32_16x16x32_f16 v[74:77], v[118:121], v[146:149], v[74:77]
	ds_read_b128 v[102:105], v159 offset:8192
	v_mfma_f32_16x16x32_f16 v[18:21], v[118:121], v[150:153], v[18:21]
	ds_read_b128 v[106:109], v159 offset:10240
	v_mfma_f32_16x16x32_f16 v[26:29], v[118:121], v[154:157], v[26:29]
	s_add_u32 m0, s11, 0xdf80
	ds_read_b128 v[110:113], v161
	global_load_lds_dwordx4 v[222:223], off offset:128
	v_mfma_f32_16x16x32_f16 v[70:73], v[122:125], v[146:149], v[70:73]
	ds_read_b128 v[114:117], v161 offset:2048
	v_mfma_f32_16x16x32_f16 v[46:49], v[122:125], v[150:153], v[46:49]
	v_mfma_f32_16x16x32_f16 v[240:243], v[122:125], v[154:157], v[240:243]
	ds_read_b128 v[118:121], v161 offset:4096
	v_mfma_f32_16x16x32_f16 v[66:69], v[126:129], v[146:149], v[66:69]
	ds_read_b128 v[122:125], v161 offset:6144
	v_mfma_f32_16x16x32_f16 v[42:45], v[126:129], v[150:153], v[42:45]
	v_mfma_f32_16x16x32_f16 v[236:239], v[126:129], v[154:157], v[236:239]
	s_add_u32 m0, s11, 0xff80
	ds_read_b128 v[126:129], v161 offset:8192
	global_load_lds_dwordx4 v[226:227], off offset:128
	v_mfma_f32_16x16x32_f16 v[62:65], v[130:133], v[146:149], v[62:65]
	v_mfma_f32_16x16x32_f16 v[38:41], v[130:133], v[150:153], v[38:41]
	v_mfma_f32_16x16x32_f16 v[34:37], v[130:133], v[154:157], v[34:37]
	ds_read_b128 v[130:133], v161 offset:10240
	ds_read_b128 v[146:149], v165
	ds_read_b128 v[150:153], v165 offset:2048
	ds_read_b128 v[154:157], v165 offset:4096
	s_waitcnt lgkmcnt(9)
	v_mfma_f32_16x16x32_f16 v[82:85], v[86:89], v[134:137], v[82:85]
	v_mfma_f32_16x16x32_f16 v[58:61], v[86:89], v[138:141], v[58:61]
	v_mfma_f32_16x16x32_f16 v[14:17], v[86:89], v[142:145], v[14:17]
	s_add_u32 m0, s11, 0x11f80
	v_mfma_f32_16x16x32_f16 v[78:81], v[90:93], v[134:137], v[78:81]
	global_load_lds_dwordx4 v[220:221], off offset:128
	v_mfma_f32_16x16x32_f16 v[22:25], v[90:93], v[138:141], v[22:25]
	v_mfma_f32_16x16x32_f16 v[30:33], v[90:93], v[142:145], v[30:33]
	v_mfma_f32_16x16x32_f16 v[74:77], v[94:97], v[134:137], v[74:77]
	v_mfma_f32_16x16x32_f16 v[18:21], v[94:97], v[138:141], v[18:21]
	v_mfma_f32_16x16x32_f16 v[26:29], v[94:97], v[142:145], v[26:29]
	s_add_u32 m0, s11, 0x13f80
	v_mfma_f32_16x16x32_f16 v[70:73], v[98:101], v[134:137], v[70:73]
	global_load_lds_dwordx4 v[224:225], off offset:128
	v_mfma_f32_16x16x32_f16 v[46:49], v[98:101], v[138:141], v[46:49]
	v_mfma_f32_16x16x32_f16 v[240:243], v[98:101], v[142:145], v[240:243]
	v_mfma_f32_16x16x32_f16 v[66:69], v[102:105], v[134:137], v[66:69]
	v_mfma_f32_16x16x32_f16 v[42:45], v[102:105], v[138:141], v[42:45]
	v_mfma_f32_16x16x32_f16 v[236:239], v[102:105], v[142:145], v[236:239]
	s_add_u32 m0, s11, 0x15f80
	v_mfma_f32_16x16x32_f16 v[62:65], v[106:109], v[134:137], v[62:65]
	global_load_lds_dwordx4 v[228:229], off offset:128
	v_mfma_f32_16x16x32_f16 v[38:41], v[106:109], v[138:141], v[38:41]
	v_mfma_f32_16x16x32_f16 v[34:37], v[106:109], v[142:145], v[34:37]
	s_waitcnt vmcnt(6) lgkmcnt(0)
	s_barrier
	ds_read_b128 v[134:137], v162
	v_mfma_f32_16x16x32_f16 v[82:85], v[110:113], v[146:149], v[82:85]
	ds_read_b128 v[138:141], v162 offset:2048
	v_mfma_f32_16x16x32_f16 v[58:61], v[110:113], v[150:153], v[58:61]
	ds_read_b128 v[142:145], v162 offset:4096
	v_mfma_f32_16x16x32_f16 v[14:17], v[110:113], v[154:157], v[14:17]
	s_add_u32 m0, s11, 0x17f00
	ds_read_b128 v[86:89], v158
	global_load_lds_dwordx4 v[218:219], off offset:256
	v_mfma_f32_16x16x32_f16 v[78:81], v[114:117], v[146:149], v[78:81]
	ds_read_b128 v[90:93], v158 offset:2048
	v_mfma_f32_16x16x32_f16 v[22:25], v[114:117], v[150:153], v[22:25]
	ds_read_b128 v[94:97], v158 offset:4096
	v_mfma_f32_16x16x32_f16 v[30:33], v[114:117], v[154:157], v[30:33]
	ds_read_b128 v[98:101], v158 offset:6144
	v_mfma_f32_16x16x32_f16 v[74:77], v[118:121], v[146:149], v[74:77]
	ds_read_b128 v[102:105], v158 offset:8192
	v_mfma_f32_16x16x32_f16 v[18:21], v[118:121], v[150:153], v[18:21]
	ds_read_b128 v[106:109], v158 offset:10240
	v_mfma_f32_16x16x32_f16 v[26:29], v[118:121], v[154:157], v[26:29]
	s_add_u32 m0, s11, 0x19f00
	ds_read_b128 v[110:113], v160
	global_load_lds_dwordx4 v[222:223], off offset:256
	v_mfma_f32_16x16x32_f16 v[70:73], v[122:125], v[146:149], v[70:73]
	ds_read_b128 v[114:117], v160 offset:2048
	v_mfma_f32_16x16x32_f16 v[46:49], v[122:125], v[150:153], v[46:49]
	v_mfma_f32_16x16x32_f16 v[240:243], v[122:125], v[154:157], v[240:243]
	ds_read_b128 v[118:121], v160 offset:4096
	v_mfma_f32_16x16x32_f16 v[66:69], v[126:129], v[146:149], v[66:69]
	ds_read_b128 v[122:125], v160 offset:6144
	v_mfma_f32_16x16x32_f16 v[42:45], v[126:129], v[150:153], v[42:45]
	v_mfma_f32_16x16x32_f16 v[236:239], v[126:129], v[154:157], v[236:239]
	s_add_u32 m0, s11, 0x1bf00
	ds_read_b128 v[126:129], v160 offset:8192
	global_load_lds_dwordx4 v[226:227], off offset:256
	v_mfma_f32_16x16x32_f16 v[62:65], v[130:133], v[146:149], v[62:65]
	v_mfma_f32_16x16x32_f16 v[38:41], v[130:133], v[150:153], v[38:41]
	v_mfma_f32_16x16x32_f16 v[34:37], v[130:133], v[154:157], v[34:37]
	ds_read_b128 v[130:133], v160 offset:10240
	ds_read_b128 v[146:149], v164
	ds_read_b128 v[150:153], v164 offset:2048
	ds_read_b128 v[154:157], v164 offset:4096
	v_lshl_add_u64 v[218:219], v[218:219], 0, s[20:21]
	v_lshl_add_u64 v[222:223], v[222:223], 0, s[20:21]
	v_lshl_add_u64 v[226:227], v[226:227], 0, s[20:21]
	v_lshl_add_u64 v[220:221], v[220:221], 0, s[20:21]
	v_lshl_add_u64 v[224:225], v[224:225], 0, s[20:21]
	v_lshl_add_u64 v[228:229], v[228:229], 0, s[20:21]
	s_sub_u32 s22, s22, 1
	s_cmp_lg_u32 s22, 0
	s_cbranch_scc1 .Lgemm_Nh_loop
	s_waitcnt lgkmcnt(9)
	v_mfma_f32_16x16x32_f16 v[82:85], v[86:89], v[134:137], v[82:85]
	v_mfma_f32_16x16x32_f16 v[58:61], v[86:89], v[138:141], v[58:61]
	v_mfma_f32_16x16x32_f16 v[14:17], v[86:89], v[142:145], v[14:17]
	s_add_u32 m0, s11, 0x1e080
	v_mfma_f32_16x16x32_f16 v[78:81], v[90:93], v[134:137], v[78:81]
	global_load_lds_dwordx4 v[220:221], off offset:-128
	v_mfma_f32_16x16x32_f16 v[22:25], v[90:93], v[138:141], v[22:25]
	v_mfma_f32_16x16x32_f16 v[30:33], v[90:93], v[142:145], v[30:33]
	v_mfma_f32_16x16x32_f16 v[74:77], v[94:97], v[134:137], v[74:77]
	v_mfma_f32_16x16x32_f16 v[18:21], v[94:97], v[138:141], v[18:21]
	v_mfma_f32_16x16x32_f16 v[26:29], v[94:97], v[142:145], v[26:29]
	s_add_u32 m0, s11, 0x20080
	v_mfma_f32_16x16x32_f16 v[70:73], v[98:101], v[134:137], v[70:73]
	global_load_lds_dwordx4 v[224:225], off offset:-128
	v_mfma_f32_16x16x32_f16 v[46:49], v[98:101], v[138:141], v[46:49]
	v_mfma_f32_16x16x32_f16 v[240:243], v[98:101], v[142:145], v[240:243]
	v_mfma_f32_16x16x32_f16 v[66:69], v[102:105], v[134:137], v[66:69]
	v_mfma_f32_16x16x32_f16 v[42:45], v[102:105], v[138:141], v[42:45]
	v_mfma_f32_16x16x32_f16 v[236:239], v[102:105], v[142:145], v[236:239]
	s_add_u32 m0, s11, 0x22080
	v_mfma_f32_16x16x32_f16 v[62:65], v[106:109], v[134:137], v[62:65]
	global_load_lds_dwordx4 v[228:229], off offset:-128
	v_mfma_f32_16x16x32_f16 v[38:41], v[106:109], v[138:141], v[38:41]
	v_mfma_f32_16x16x32_f16 v[34:37], v[106:109], v[142:145], v[34:37]
	s_waitcnt vmcnt(6) lgkmcnt(0)
	s_barrier
	ds_read_b128 v[134:137], v162 offset:49152
	v_mfma_f32_16x16x32_f16 v[82:85], v[110:113], v[146:149], v[82:85]
	ds_read_b128 v[138:141], v162 offset:51200
	v_mfma_f32_16x16x32_f16 v[58:61], v[110:113], v[150:153], v[58:61]
	ds_read_b128 v[142:145], v162 offset:53248
	v_mfma_f32_16x16x32_f16 v[14:17], v[110:113], v[154:157], v[14:17]
	s_add_u32 m0, s11, 0x0
	ds_read_b128 v[86:89], v158 offset:49152
	global_load_lds_dwordx4 v[218:219], off
	v_mfma_f32_16x16x32_f16 v[78:81], v[114:117], v[146:149], v[78:81]
	ds_read_b128 v[90:93], v158 offset:51200
	v_mfma_f32_16x16x32_f16 v[22:25], v[114:117], v[150:153], v[22:25]
	ds_read_b128 v[94:97], v158 offset:53248
	v_mfma_f32_16x16x32_f16 v[30:33], v[114:117], v[154:157], v[30:33]
	ds_read_b128 v[98:101], v158 offset:55296
	v_mfma_f32_16x16x32_f16 v[74:77], v[118:121], v[146:149], v[74:77]
	ds_read_b128 v[102:105], v158 offset:57344
	v_mfma_f32_16x16x32_f16 v[18:21], v[118:121], v[150:153], v[18:21]
	ds_read_b128 v[106:109], v158 offset:59392
	v_mfma_f32_16x16x32_f16 v[26:29], v[118:121], v[154:157], v[26:29]
	s_add_u32 m0, s11, 0x2000
	ds_read_b128 v[110:113], v160 offset:49152
	global_load_lds_dwordx4 v[222:223], off
	v_mfma_f32_16x16x32_f16 v[70:73], v[122:125], v[146:149], v[70:73]
	ds_read_b128 v[114:117], v160 offset:51200
	v_mfma_f32_16x16x32_f16 v[46:49], v[122:125], v[150:153], v[46:49]
	v_mfma_f32_16x16x32_f16 v[240:243], v[122:125], v[154:157], v[240:243]
	ds_read_b128 v[118:121], v160 offset:53248
	v_mfma_f32_16x16x32_f16 v[66:69], v[126:129], v[146:149], v[66:69]
	ds_read_b128 v[122:125], v160 offset:55296
	v_mfma_f32_16x16x32_f16 v[42:45], v[126:129], v[150:153], v[42:45]
	v_mfma_f32_16x16x32_f16 v[236:239], v[126:129], v[154:157], v[236:239]
	s_add_u32 m0, s11, 0x4000
	ds_read_b128 v[126:129], v160 offset:57344
	global_load_lds_dwordx4 v[226:227], off
	v_mfma_f32_16x16x32_f16 v[62:65], v[130:133], v[146:149], v[62:65]
	v_mfma_f32_16x16x32_f16 v[38:41], v[130:133], v[150:153], v[38:41]
	v_mfma_f32_16x16x32_f16 v[34:37], v[130:133], v[154:157], v[34:37]
	ds_read_b128 v[130:133], v160 offset:59392
	ds_read_b128 v[146:149], v164 offset:49152
	ds_read_b128 v[150:153], v164 offset:51200
	ds_read_b128 v[154:157], v164 offset:53248
	s_waitcnt lgkmcnt(9)
	v_mfma_f32_16x16x32_f16 v[82:85], v[86:89], v[134:137], v[82:85]
	v_mfma_f32_16x16x32_f16 v[58:61], v[86:89], v[138:141], v[58:61]
	v_mfma_f32_16x16x32_f16 v[14:17], v[86:89], v[142:145], v[14:17]
	s_add_u32 m0, s11, 0x6000
	v_mfma_f32_16x16x32_f16 v[78:81], v[90:93], v[134:137], v[78:81]
	global_load_lds_dwordx4 v[220:221], off
	v_mfma_f32_16x16x32_f16 v[22:25], v[90:93], v[138:141], v[22:25]
	v_mfma_f32_16x16x32_f16 v[30:33], v[90:93], v[142:145], v[30:33]
	v_mfma_f32_16x16x32_f16 v[74:77], v[94:97], v[134:137], v[74:77]
	v_mfma_f32_16x16x32_f16 v[18:21], v[94:97], v[138:141], v[18:21]
	v_mfma_f32_16x16x32_f16 v[26:29], v[94:97], v[142:145], v[26:29]
	s_add_u32 m0, s11, 0x8000
	v_mfma_f32_16x16x32_f16 v[70:73], v[98:101], v[134:137], v[70:73]
	global_load_lds_dwordx4 v[224:225], off
	v_mfma_f32_16x16x32_f16 v[46:49], v[98:101], v[138:141], v[46:49]
	v_mfma_f32_16x16x32_f16 v[240:243], v[98:101], v[142:145], v[240:243]
	v_mfma_f32_16x16x32_f16 v[66:69], v[102:105], v[134:137], v[66:69]
	v_mfma_f32_16x16x32_f16 v[42:45], v[102:105], v[138:141], v[42:45]
	v_mfma_f32_16x16x32_f16 v[236:239], v[102:105], v[142:145], v[236:239]
	s_add_u32 m0, s11, 0xa000
	v_mfma_f32_16x16x32_f16 v[62:65], v[106:109], v[134:137], v[62:65]
	global_load_lds_dwordx4 v[228:229], off
	v_mfma_f32_16x16x32_f16 v[38:41], v[106:109], v[138:141], v[38:41]
	v_mfma_f32_16x16x32_f16 v[34:37], v[106:109], v[142:145], v[34:37]
	s_waitcnt vmcnt(6) lgkmcnt(0)
	s_barrier
	s_lshl_b32 s26, s17, 2
	s_add_u32 s26, s24, s26
	s_addc_u32 s27, s25, 0
	v_lshlrev_b32_e32 v50, 2, v1
	global_load_dword v234, v50, s[26:27]
	global_load_dword v232, v50, s[26:27] offset:64
	global_load_dword v230, v50, s[26:27] offset:128
	ds_read_b128 v[134:137], v163
	v_mfma_f32_16x16x32_f16 v[82:85], v[110:113], v[146:149], v[82:85]
	ds_read_b128 v[138:141], v163 offset:2048
	v_mfma_f32_16x16x32_f16 v[58:61], v[110:113], v[150:153], v[58:61]
	ds_read_b128 v[142:145], v163 offset:4096
	v_mfma_f32_16x16x32_f16 v[14:17], v[110:113], v[154:157], v[14:17]
	ds_read_b128 v[86:89], v159
	v_mfma_f32_16x16x32_f16 v[78:81], v[114:117], v[146:149], v[78:81]
	ds_read_b128 v[90:93], v159 offset:2048
	v_mfma_f32_16x16x32_f16 v[22:25], v[114:117], v[150:153], v[22:25]
	ds_read_b128 v[94:97], v159 offset:4096
	v_mfma_f32_16x16x32_f16 v[30:33], v[114:117], v[154:157], v[30:33]
	ds_read_b128 v[98:101], v159 offset:6144
	v_mfma_f32_16x16x32_f16 v[74:77], v[118:121], v[146:149], v[74:77]
	ds_read_b128 v[102:105], v159 offset:8192
	v_mfma_f32_16x16x32_f16 v[18:21], v[118:121], v[150:153], v[18:21]
	ds_read_b128 v[106:109], v159 offset:10240
	v_mfma_f32_16x16x32_f16 v[26:29], v[118:121], v[154:157], v[26:29]
	ds_read_b128 v[110:113], v161
	v_mfma_f32_16x16x32_f16 v[70:73], v[122:125], v[146:149], v[70:73]
	ds_read_b128 v[114:117], v161 offset:2048
	v_mfma_f32_16x16x32_f16 v[46:49], v[122:125], v[150:153], v[46:49]
	v_mfma_f32_16x16x32_f16 v[240:243], v[122:125], v[154:157], v[240:243]
	ds_read_b128 v[118:121], v161 offset:4096
	v_mfma_f32_16x16x32_f16 v[66:69], v[126:129], v[146:149], v[66:69]
	ds_read_b128 v[122:125], v161 offset:6144
	v_mfma_f32_16x16x32_f16 v[42:45], v[126:129], v[150:153], v[42:45]
	v_mfma_f32_16x16x32_f16 v[236:239], v[126:129], v[154:157], v[236:239]
	ds_read_b128 v[126:129], v161 offset:8192
	v_mfma_f32_16x16x32_f16 v[62:65], v[130:133], v[146:149], v[62:65]
	v_mfma_f32_16x16x32_f16 v[38:41], v[130:133], v[150:153], v[38:41]
	v_mfma_f32_16x16x32_f16 v[34:37], v[130:133], v[154:157], v[34:37]
	ds_read_b128 v[130:133], v161 offset:10240
	ds_read_b128 v[146:149], v165
	ds_read_b128 v[150:153], v165 offset:2048
	ds_read_b128 v[154:157], v165 offset:4096
	s_waitcnt lgkmcnt(9)
	v_mfma_f32_16x16x32_f16 v[82:85], v[86:89], v[134:137], v[82:85]
	v_mfma_f32_16x16x32_f16 v[58:61], v[86:89], v[138:141], v[58:61]
	v_mfma_f32_16x16x32_f16 v[14:17], v[86:89], v[142:145], v[14:17]
	v_mfma_f32_16x16x32_f16 v[78:81], v[90:93], v[134:137], v[78:81]
	v_mfma_f32_16x16x32_f16 v[22:25], v[90:93], v[138:141], v[22:25]
	v_mfma_f32_16x16x32_f16 v[30:33], v[90:93], v[142:145], v[30:33]
	v_mfma_f32_16x16x32_f16 v[74:77], v[94:97], v[134:137], v[74:77]
	v_mfma_f32_16x16x32_f16 v[18:21], v[94:97], v[138:141], v[18:21]
	v_mfma_f32_16x16x32_f16 v[26:29], v[94:97], v[142:145], v[26:29]
	v_mfma_f32_16x16x32_f16 v[70:73], v[98:101], v[134:137], v[70:73]
	v_mfma_f32_16x16x32_f16 v[46:49], v[98:101], v[138:141], v[46:49]
	v_mfma_f32_16x16x32_f16 v[240:243], v[98:101], v[142:145], v[240:243]
	v_mfma_f32_16x16x32_f16 v[66:69], v[102:105], v[134:137], v[66:69]
	v_mfma_f32_16x16x32_f16 v[42:45], v[102:105], v[138:141], v[42:45]
	v_mfma_f32_16x16x32_f16 v[236:239], v[102:105], v[142:145], v[236:239]
	v_mfma_f32_16x16x32_f16 v[62:65], v[106:109], v[134:137], v[62:65]
	v_mfma_f32_16x16x32_f16 v[38:41], v[106:109], v[138:141], v[38:41]
	v_mfma_f32_16x16x32_f16 v[34:37], v[106:109], v[142:145], v[34:37]
	s_waitcnt vmcnt(3) lgkmcnt(0)
	s_barrier
	ds_read_b128 v[134:137], v162
	v_mfma_f32_16x16x32_f16 v[82:85], v[110:113], v[146:149], v[82:85]
	ds_read_b128 v[138:141], v162 offset:2048
	v_mfma_f32_16x16x32_f16 v[58:61], v[110:113], v[150:153], v[58:61]
	ds_read_b128 v[142:145], v162 offset:4096
	v_mfma_f32_16x16x32_f16 v[14:17], v[110:113], v[154:157], v[14:17]
	ds_read_b128 v[86:89], v158
	v_mfma_f32_16x16x32_f16 v[78:81], v[114:117], v[146:149], v[78:81]
	ds_read_b128 v[90:93], v158 offset:2048
	v_mfma_f32_16x16x32_f16 v[22:25], v[114:117], v[150:153], v[22:25]
	ds_read_b128 v[94:97], v158 offset:4096
	v_mfma_f32_16x16x32_f16 v[30:33], v[114:117], v[154:157], v[30:33]
	ds_read_b128 v[98:101], v158 offset:6144
	v_mfma_f32_16x16x32_f16 v[74:77], v[118:121], v[146:149], v[74:77]
	ds_read_b128 v[102:105], v158 offset:8192
	v_mfma_f32_16x16x32_f16 v[18:21], v[118:121], v[150:153], v[18:21]
	ds_read_b128 v[106:109], v158 offset:10240
	v_mfma_f32_16x16x32_f16 v[26:29], v[118:121], v[154:157], v[26:29]
	ds_read_b128 v[110:113], v160
	v_mfma_f32_16x16x32_f16 v[70:73], v[122:125], v[146:149], v[70:73]
	ds_read_b128 v[114:117], v160 offset:2048
	v_mfma_f32_16x16x32_f16 v[46:49], v[122:125], v[150:153], v[46:49]
	v_mfma_f32_16x16x32_f16 v[240:243], v[122:125], v[154:157], v[240:243]
	ds_read_b128 v[118:121], v160 offset:4096
	v_mfma_f32_16x16x32_f16 v[66:69], v[126:129], v[146:149], v[66:69]
	ds_read_b128 v[122:125], v160 offset:6144
	v_mfma_f32_16x16x32_f16 v[42:45], v[126:129], v[150:153], v[42:45]
	v_mfma_f32_16x16x32_f16 v[236:239], v[126:129], v[154:157], v[236:239]
	ds_read_b128 v[126:129], v160 offset:8192
	v_mfma_f32_16x16x32_f16 v[62:65], v[130:133], v[146:149], v[62:65]
	v_mfma_f32_16x16x32_f16 v[38:41], v[130:133], v[150:153], v[38:41]
	v_mfma_f32_16x16x32_f16 v[34:37], v[130:133], v[154:157], v[34:37]
	ds_read_b128 v[130:133], v160 offset:10240
	ds_read_b128 v[146:149], v164
	ds_read_b128 v[150:153], v164 offset:2048
	ds_read_b128 v[154:157], v164 offset:4096
	s_waitcnt lgkmcnt(9)
	v_mfma_f32_16x16x32_f16 v[82:85], v[86:89], v[134:137], v[82:85]
	v_mfma_f32_16x16x32_f16 v[58:61], v[86:89], v[138:141], v[58:61]
	v_mfma_f32_16x16x32_f16 v[14:17], v[86:89], v[142:145], v[14:17]
	v_mfma_f32_16x16x32_f16 v[78:81], v[90:93], v[134:137], v[78:81]
	v_mfma_f32_16x16x32_f16 v[22:25], v[90:93], v[138:141], v[22:25]
	v_mfma_f32_16x16x32_f16 v[30:33], v[90:93], v[142:145], v[30:33]
	v_mfma_f32_16x16x32_f16 v[74:77], v[94:97], v[134:137], v[74:77]
	v_mfma_f32_16x16x32_f16 v[18:21], v[94:97], v[138:141], v[18:21]
	v_mfma_f32_16x16x32_f16 v[26:29], v[94:97], v[142:145], v[26:29]
	v_mfma_f32_16x16x32_f16 v[70:73], v[98:101], v[134:137], v[70:73]
	v_mfma_f32_16x16x32_f16 v[46:49], v[98:101], v[138:141], v[46:49]
	v_mfma_f32_16x16x32_f16 v[240:243], v[98:101], v[142:145], v[240:243]
	v_mfma_f32_16x16x32_f16 v[66:69], v[102:105], v[134:137], v[66:69]
	v_mfma_f32_16x16x32_f16 v[42:45], v[102:105], v[138:141], v[42:45]
	v_mfma_f32_16x16x32_f16 v[236:239], v[102:105], v[142:145], v[236:239]
	v_mfma_f32_16x16x32_f16 v[62:65], v[106:109], v[134:137], v[62:65]
	v_mfma_f32_16x16x32_f16 v[38:41], v[106:109], v[138:141], v[38:41]
	v_mfma_f32_16x16x32_f16 v[34:37], v[106:109], v[142:145], v[34:37]
	s_waitcnt lgkmcnt(0)
	v_mfma_f32_16x16x32_f16 v[82:85], v[110:113], v[146:149], v[82:85]
	v_mfma_f32_16x16x32_f16 v[58:61], v[110:113], v[150:153], v[58:61]
	v_mfma_f32_16x16x32_f16 v[14:17], v[110:113], v[154:157], v[14:17]
	v_mfma_f32_16x16x32_f16 v[78:81], v[114:117], v[146:149], v[78:81]
	v_mfma_f32_16x16x32_f16 v[22:25], v[114:117], v[150:153], v[22:25]
	v_mfma_f32_16x16x32_f16 v[30:33], v[114:117], v[154:157], v[30:33]
	v_mfma_f32_16x16x32_f16 v[74:77], v[118:121], v[146:149], v[74:77]
	v_mfma_f32_16x16x32_f16 v[18:21], v[118:121], v[150:153], v[18:21]
	v_mfma_f32_16x16x32_f16 v[26:29], v[118:121], v[154:157], v[26:29]
	v_mfma_f32_16x16x32_f16 v[70:73], v[122:125], v[146:149], v[70:73]
	v_mfma_f32_16x16x32_f16 v[46:49], v[122:125], v[150:153], v[46:49]
	v_mfma_f32_16x16x32_f16 v[240:243], v[122:125], v[154:157], v[240:243]
	v_mfma_f32_16x16x32_f16 v[66:69], v[126:129], v[146:149], v[66:69]
	v_mfma_f32_16x16x32_f16 v[42:45], v[126:129], v[150:153], v[42:45]
	v_mfma_f32_16x16x32_f16 v[236:239], v[126:129], v[154:157], v[236:239]
	v_mfma_f32_16x16x32_f16 v[62:65], v[130:133], v[146:149], v[62:65]
	v_mfma_f32_16x16x32_f16 v[38:41], v[130:133], v[150:153], v[38:41]
	v_mfma_f32_16x16x32_f16 v[34:37], v[130:133], v[154:157], v[34:37]
